# batched counter loads in MoE prefix setup; head-major int8 attention partials; hoisted row-scale loads (gate GEMM epilogue); preloaded column scales (k-mean epilogue); no store drain at attention-B un
# speedup vs baseline: 1.0159x; 1.0036x over previous
.LBB0_125:
	s_ashr_i32 s46, s10, 2
	s_ashr_i32 s47, s46, 31
	v_cvt_f32_i32_e32 v204, v86
	v_cvt_f32_i32_e32 v86, v58
	v_cvt_f32_i32_e32 v58, v6
	v_mov_b32_e32 v6, 0
	s_lshl_b64 s[48:49], s[46:47], 26
	s_and_b32 s31, s10, 3
	s_lshl_b32 s35, s44, 8
	v_cvt_f32_i32_e32 v170, v104
	v_cvt_f32_i32_e32 v104, v52
	v_cvt_f32_i32_e32 v171, v105
	v_add3_u32 v52, s35, v159, v6
	s_add_u32 s35, s40, s48
	v_cvt_f32_i32_e32 v162, v70
	v_cvt_f32_i32_e32 v105, v53
	v_cvt_f32_i32_e32 v70, v42
	v_mov_b32_e32 v42, 0
	v_ashrrev_i32_e32 v53, 31, v52
	s_addc_u32 s45, s41, s49
	s_lshl_b32 s10, s10, 8
	v_cvt_f32_i32_e32 v205, v87
	v_cvt_f32_i32_e32 v210, v88
	v_cvt_f32_i32_e32 v88, v62
	v_cvt_f32_i32_e32 v87, v59
	v_cvt_f32_i32_e32 v62, v50
	v_cvt_f32_i32_e32 v59, v7
	v_lshl_add_u64 v[6:7], v[52:53], 2, s[14:15]
	v_add_lshl_u32 v50, v42, v1, 3
	s_or_b32 s47, s10, s60
	s_lshl_b64 s[48:49], s[10:11], 2
	s_add_u32 s48, s64, s48
	s_addc_u32 s49, s65, s49
	v_ashrrev_i32_e32 v253, 31, v50
	v_mov_b32_e32 v252, v50
	v_lshl_add_u64 v[252:253], v[252:253], 2, s[48:49]
	global_load_dwordx4 v[236:239], v[252:253], off
	global_load_dwordx4 v[240:243], v[252:253], off offset:16
	global_load_dwordx4 v[244:247], v[252:253], off offset:512
	global_load_dwordx4 v[248:251], v[252:253], off offset:528
	v_cvt_f32_i32_e32 v150, v64
	v_cvt_f32_i32_e32 v64, v54
	global_load_dword v54, v[6:7], off
	v_add_u32_e32 v6, s47, v50
	v_ashrrev_i32_e32 v7, 31, v6
	v_cvt_f32_i32_e32 v154, v112
	v_cvt_f32_i32_e32 v112, v90
	v_cvt_f32_i32_e32 v189, v77
	v_cvt_f32_i32_e32 v188, v76
	v_cvt_f32_i32_e32 v77, v47
	v_cvt_f32_i32_e32 v76, v46
	v_lshl_add_u64 v[46:47], v[6:7], 2, s[16:17]
	v_cvt_f32_i32_e32 v90, v2
	v_add_u32_e32 v2, 0x80, v6
	v_cvt_f32_i32_e32 v155, v113
	v_cvt_f32_i32_e32 v113, v91
	v_cvt_f32_i32_e32 v187, v79
	v_cvt_f32_i32_e32 v186, v78
	v_cvt_f32_i32_e32 v195, v81
	v_cvt_f32_i32_e32 v194, v80
	v_cvt_f32_i32_e32 v163, v71
	v_cvt_f32_i32_e32 v81, v49
	v_cvt_f32_i32_e32 v80, v48
	v_cvt_f32_i32_e32 v71, v43
	v_cvt_f32_i32_e32 v79, v45
	v_cvt_f32_i32_e32 v78, v44
	global_load_dwordx4 v[42:45], v[46:47], off offset:16
	s_nop 0
	global_load_dwordx4 v[46:49], v[46:47], off
	v_cvt_f32_i32_e32 v91, v3
	v_ashrrev_i32_e32 v3, 31, v2
	v_cvt_f32_i32_e32 v196, v40
	v_lshl_add_u64 v[6:7], v[2:3], 2, s[16:17]
	v_cvt_f32_i32_e32 v40, v30
	v_add_u32_e32 v30, 16, v52
	v_cvt_f32_i32_e32 v209, v117
	v_cvt_f32_i32_e32 v208, v116
	v_cvt_f32_i32_e32 v221, v97
	v_cvt_f32_i32_e32 v220, v96
	v_cvt_f32_i32_e32 v117, v93
	v_cvt_f32_i32_e32 v116, v92
	v_cvt_f32_i32_e32 v97, v9
	v_cvt_f32_i32_e32 v96, v8
	v_cvt_f32_i32_e32 v93, v5
	v_cvt_f32_i32_e32 v92, v4
	v_cvt_f32_i32_e32 v197, v41
	v_cvt_f32_i32_e32 v41, v31
	global_load_dwordx4 v[2:5], v[6:7], off offset:16
	s_nop 0
	global_load_dwordx4 v[6:9], v[6:7], off
	v_ashrrev_i32_e32 v31, 31, v30
	v_cvt_f32_i32_e32 v173, v11
	v_cvt_f32_i32_e32 v172, v10
	v_lshl_add_u64 v[10:11], v[30:31], 2, s[14:15]
	v_cvt_f32_i32_e32 v160, v66
	global_load_dword v66, v[10:11], off
	v_cvt_f32_i32_e32 v206, v118
	v_cvt_f32_i32_e32 v118, v18
	v_add_u32_e32 v18, 32, v52
	v_cvt_f32_i32_e32 v207, v119
	v_cvt_f32_i32_e32 v119, v19
	v_ashrrev_i32_e32 v19, 31, v18
	v_lshl_add_u64 v[10:11], v[18:19], 2, s[14:15]
	v_cvt_f32_i32_e32 v156, v110
	v_cvt_f32_i32_e32 v110, v98
	v_cvt_f32_i32_e32 v98, v22
	global_load_dword v22, v[10:11], off
	v_cvt_f32_i32_e32 v218, v94
	v_cvt_f32_i32_e32 v94, v26
	v_add_u32_e32 v26, 48, v52
	v_cvt_f32_i32_e32 v222, v124
	v_cvt_f32_i32_e32 v219, v95
	v_cvt_f32_i32_e32 v95, v27
	v_ashrrev_i32_e32 v27, 31, v26
	v_add_u32_e32 v216, 0x80, v52
	v_add_u32_e32 v200, 0x90, v52
	v_add_u32_e32 v180, 0xa0, v52
	v_add_u32_e32 v124, 0xb0, v52
	v_cvt_f32_i32_e32 v223, v125
	v_lshl_add_u64 v[10:11], v[26:27], 2, s[14:15]
	v_ashrrev_i32_e32 v217, 31, v216
	v_ashrrev_i32_e32 v201, 31, v200
	v_ashrrev_i32_e32 v181, 31, v180
	v_ashrrev_i32_e32 v125, 31, v124
	v_cvt_f32_i32_e32 v225, v127
	v_cvt_f32_i32_e32 v224, v126
	v_cvt_f32_i32_e32 v153, v123
	v_cvt_f32_i32_e32 v152, v122
	v_cvt_f32_i32_e32 v213, v121
	v_cvt_f32_i32_e32 v212, v120
	v_cvt_f32_i32_e32 v202, v114
	v_cvt_f32_i32_e32 v166, v100
	v_cvt_f32_i32_e32 v177, v13
	v_cvt_f32_i32_e32 v176, v12
	v_cvt_f32_i32_e32 v121, v15
	v_cvt_f32_i32_e32 v120, v14
	v_cvt_f32_i32_e32 v127, v17
	v_cvt_f32_i32_e32 v126, v16
	v_cvt_f32_i32_e32 v123, v21
	v_cvt_f32_i32_e32 v122, v20
	v_cvt_f32_i32_e32 v100, v28
	v_lshl_add_u64 v[12:13], v[216:217], 2, s[14:15]
	v_lshl_add_u64 v[14:15], v[200:201], 2, s[14:15]
	v_lshl_add_u64 v[16:17], v[180:181], 2, s[14:15]
	v_lshl_add_u64 v[20:21], v[124:125], 2, s[14:15]
	global_load_dword v28, v[10:11], off
	global_load_dword v214, v[12:13], off
	global_load_dword v190, v[14:15], off
	global_load_dword v158, v[16:17], off
	global_load_dword v114, v[20:21], off
	v_cvt_f32_i32_e32 v227, v129
	v_cvt_f32_i32_e32 v226, v128
	s_lshl_b32 s47, s31, 9
	s_add_u32 s48, s35, s47
	v_cvt_f32_i32_e32 v183, v75
	v_cvt_f32_i32_e32 v182, v74
	v_cvt_f32_i32_e32 v169, v73
	v_cvt_f32_i32_e32 v168, v72
	v_cvt_f32_i32_e32 v179, v37
	v_cvt_f32_i32_e32 v178, v36
	s_addc_u32 s49, s45, 0
	v_add_u32_e32 v14, s60, v50
	v_lshlrev_b64 v[10:11], 11, v[52:53]
	s_waitcnt vmcnt(0)
	v_pk_mul_f32 v[72:73], v[54:55], v[226:227] op_sel_hi:[0,1]
	v_pk_mul_f32 v[74:75], v[54:55], v[224:225] op_sel_hi:[0,1]
	v_pk_mul_f32 v[36:37], v[54:55], v[152:153] op_sel_hi:[0,1]
	v_cvt_f32_i32_e32 v193, v109
	v_cvt_f32_i32_e32 v192, v108
	v_cvt_f32_i32_e32 v109, v103
	v_cvt_f32_i32_e32 v108, v102
	v_cvt_f32_i32_e32 v175, v35
	v_cvt_f32_i32_e32 v174, v34
	v_cvt_f32_i32_e32 v103, v25
	v_cvt_f32_i32_e32 v102, v24
	v_lshl_add_u64 v[16:17], s[48:49], 0, v[10:11]
	v_pk_mul_f32 v[12:13], v[72:73], v[48:49]
	v_pk_mul_f32 v[10:11], v[74:75], v[46:47]
	v_pk_mul_f32 v[34:35], v[54:55], v[222:223] op_sel_hi:[0,1]
	v_pk_mul_f32 v[24:25], v[36:37], v[42:43]
	v_ashrrev_i32_e32 v15, 31, v14
	v_cvt_f32_i32_e32 v203, v115
	v_pk_mul_f32 v[20:21], v[34:35], v[44:45]
	v_cvt_pk_bf16_f32 v10, v10, v11
	v_cvt_pk_bf16_f32 v11, v12, v13
	v_cvt_pk_bf16_f32 v12, v24, v25
	v_lshlrev_b64 v[152:153], 1, v[14:15]
	v_pk_mul_f32 v[24:25], v[54:55], v[218:219] op_sel_hi:[0,1]
	v_cvt_f32_i32_e32 v211, v89
	v_cvt_f32_i32_e32 v199, v33
	v_cvt_f32_i32_e32 v198, v32
	v_cvt_pk_bf16_f32 v13, v20, v21
	v_lshl_add_u64 v[32:33], v[16:17], 0, v[152:153]
	v_pk_mul_f32 v[20:21], v[54:55], v[220:221] op_sel_hi:[0,1]
	v_pk_mul_f32 v[14:15], v[24:25], v[6:7]
	v_cvt_f32_i32_e32 v83, v83
	v_cvt_f32_i32_e32 v82, v82
	v_cvt_f32_i32_e32 v85, v85
	v_cvt_f32_i32_e32 v84, v84
	global_store_dwordx4 v[32:33], v[10:13], off
	v_pk_mul_f32 v[16:17], v[20:21], v[8:9]
	v_cvt_pk_bf16_f32 v14, v14, v15
	v_cvt_f32_i32_e32 v157, v111
	v_pk_mul_f32 v[10:11], v[54:55], v[116:117] op_sel_hi:[0,1]
	v_pk_mul_f32 v[12:13], v[54:55], v[112:113] op_sel_hi:[0,1]
	v_cvt_pk_bf16_f32 v15, v16, v17
	v_cvt_f32_i32_e32 v185, v107
	v_cvt_f32_i32_e32 v184, v106
	v_cvt_f32_i32_e32 v151, v65
	v_cvt_f32_i32_e32 v65, v55
	v_cvt_f32_i32_e32 v107, v57
	v_cvt_f32_i32_e32 v106, v56
	v_pk_mul_f32 v[52:53], v[10:11], v[4:5]
	v_pk_mul_f32 v[54:55], v[12:13], v[2:3]
	v_pk_mul_f32 v[112:113], v[66:67], v[212:213] op_sel_hi:[0,1]
	v_cvt_pk_bf16_f32 v16, v54, v55
	v_cvt_pk_bf16_f32 v17, v52, v53
	global_store_dwordx4 v[32:33], v[14:17], off offset:256
	v_pk_mul_f32 v[116:117], v[66:67], v[206:207] op_sel_hi:[0,1]
	v_pk_mul_f32 v[56:57], v[66:67], v[208:209] op_sel_hi:[0,1]
	v_lshlrev_b64 v[14:15], 11, v[30:31]
	v_cvt_f32_i32_e32 v129, v61
	v_cvt_f32_i32_e32 v128, v60
	v_lshl_add_u64 v[30:31], s[48:49], 0, v[14:15]
	v_pk_mul_f32 v[16:17], v[112:113], v[48:49]
	v_pk_mul_f32 v[14:15], v[116:117], v[46:47]
	v_pk_mul_f32 v[60:61], v[66:67], v[202:203] op_sel_hi:[0,1]
	v_pk_mul_f32 v[32:33], v[56:57], v[44:45]
	v_cvt_f32_i32_e32 v165, v69
	v_cvt_f32_i32_e32 v164, v68
	v_pk_mul_f32 v[52:53], v[60:61], v[42:43]
	v_cvt_pk_bf16_f32 v14, v14, v15
	v_cvt_pk_bf16_f32 v15, v16, v17
	v_lshl_add_u64 v[68:69], v[30:31], 0, v[152:153]
	v_cvt_pk_bf16_f32 v16, v52, v53
	v_cvt_pk_bf16_f32 v17, v32, v33
	v_pk_mul_f32 v[30:31], v[66:67], v[210:211] op_sel_hi:[0,1]
	v_pk_mul_f32 v[32:33], v[66:67], v[204:205] op_sel_hi:[0,1]
	global_store_dwordx4 v[68:69], v[14:17], off
	v_pk_mul_f32 v[54:55], v[30:31], v[8:9]
	v_pk_mul_f32 v[52:53], v[32:33], v[6:7]
	v_pk_mul_f32 v[14:15], v[66:67], v[84:85] op_sel_hi:[0,1]
	v_pk_mul_f32 v[16:17], v[66:67], v[82:83] op_sel_hi:[0,1]
	v_cvt_f32_i32_e32 v161, v67
	v_pk_mul_f32 v[66:67], v[14:15], v[4:5]
	v_pk_mul_f32 v[82:83], v[16:17], v[2:3]
	v_cvt_pk_bf16_f32 v52, v52, v53
	v_cvt_pk_bf16_f32 v53, v54, v55
	v_lshlrev_b64 v[18:19], 11, v[18:19]
	v_cvt_pk_bf16_f32 v54, v82, v83
	v_cvt_pk_bf16_f32 v55, v66, v67
	v_pk_mul_f32 v[154:155], v[22:23], v[154:155] op_sel_hi:[0,1]
	v_pk_mul_f32 v[156:157], v[22:23], v[156:157] op_sel_hi:[0,1]
	v_cvt_f32_i32_e32 v167, v101
	global_store_dwordx4 v[68:69], v[52:55], off offset:256
	v_lshl_add_u64 v[18:19], s[48:49], 0, v[18:19]
	v_pk_mul_f32 v[82:83], v[22:23], v[192:193] op_sel_hi:[0,1]
	v_pk_mul_f32 v[54:55], v[154:155], v[48:49]
	v_pk_mul_f32 v[52:53], v[156:157], v[46:47]
	v_pk_mul_f32 v[84:85], v[22:23], v[184:185] op_sel_hi:[0,1]
	v_cvt_f32_i32_e32 v111, v99
	v_pk_mul_f32 v[66:67], v[82:83], v[44:45]
	v_pk_mul_f32 v[68:69], v[84:85], v[42:43]
	v_cvt_pk_bf16_f32 v52, v52, v53
	v_cvt_pk_bf16_f32 v53, v54, v55
	v_lshl_add_u64 v[184:185], v[18:19], 0, v[152:153]
	v_cvt_pk_bf16_f32 v54, v68, v69
	v_cvt_pk_bf16_f32 v55, v66, v67
	global_store_dwordx4 v[184:185], v[52:55], off
	v_pk_mul_f32 v[18:19], v[22:23], v[188:189] op_sel_hi:[0,1]
	v_cvt_f32_i32_e32 v99, v23
	v_pk_mul_f32 v[52:53], v[22:23], v[194:195] op_sel_hi:[0,1]
	v_pk_mul_f32 v[54:55], v[22:23], v[186:187] op_sel_hi:[0,1]
	v_pk_mul_f32 v[68:69], v[52:53], v[8:9]
	v_pk_mul_f32 v[66:67], v[54:55], v[6:7]
	v_pk_mul_f32 v[22:23], v[22:23], v[182:183] op_sel_hi:[0,1]
	v_pk_mul_f32 v[182:183], v[18:19], v[4:5]
	v_pk_mul_f32 v[186:187], v[22:23], v[2:3]
	v_cvt_pk_bf16_f32 v66, v66, v67
	v_cvt_pk_bf16_f32 v67, v68, v69
	v_lshlrev_b64 v[26:27], 11, v[26:27]
	v_cvt_pk_bf16_f32 v68, v186, v187
	v_cvt_pk_bf16_f32 v69, v182, v183
	v_pk_mul_f32 v[170:171], v[28:29], v[170:171] op_sel_hi:[0,1]
	v_pk_mul_f32 v[182:183], v[28:29], v[108:109] op_sel_hi:[0,1]
	v_pk_mul_f32 v[108:109], v[28:29], v[166:167] op_sel_hi:[0,1]
	global_store_dwordx4 v[184:185], v[66:69], off offset:256
	v_lshl_add_u64 v[26:27], s[48:49], 0, v[26:27]
	v_pk_mul_f32 v[110:111], v[28:29], v[110:111] op_sel_hi:[0,1]
	v_pk_mul_f32 v[68:69], v[170:171], v[48:49]
	v_pk_mul_f32 v[66:67], v[182:183], v[46:47]
	v_pk_mul_f32 v[166:167], v[108:109], v[44:45]
	v_cvt_f32_i32_e32 v89, v63
	v_pk_mul_f32 v[184:185], v[110:111], v[42:43]
	v_cvt_pk_bf16_f32 v66, v66, v67
	v_cvt_pk_bf16_f32 v67, v68, v69
	v_cvt_f32_i32_e32 v39, v39
	v_cvt_pk_bf16_f32 v68, v184, v185
	v_cvt_pk_bf16_f32 v69, v166, v167
	v_lshl_add_u64 v[166:167], v[26:27], 0, v[152:153]
	global_store_dwordx4 v[166:167], v[66:69], off
	v_cvt_f32_i32_e32 v38, v38
	v_cvt_f32_i32_e32 v101, v29
	v_pk_mul_f32 v[66:67], v[28:29], v[168:169] op_sel_hi:[0,1]
	v_pk_mul_f32 v[68:69], v[28:29], v[162:163] op_sel_hi:[0,1]
	v_pk_mul_f32 v[162:163], v[66:67], v[8:9]
	v_pk_mul_f32 v[168:169], v[68:69], v[6:7]
	v_pk_mul_f32 v[26:27], v[28:29], v[164:165] op_sel_hi:[0,1]
	v_pk_mul_f32 v[28:29], v[28:29], v[160:161] op_sel_hi:[0,1]
	v_cvt_pk_bf16_f32 v160, v168, v169
	v_cvt_pk_bf16_f32 v161, v162, v163
	v_pk_mul_f32 v[164:165], v[26:27], v[4:5]
	v_pk_mul_f32 v[184:185], v[28:29], v[2:3]
	v_pk_mul_f32 v[168:169], v[214:215], v[150:151] op_sel_hi:[0,1]
	v_cvt_pk_bf16_f32 v162, v184, v185
	v_cvt_pk_bf16_f32 v163, v164, v165
	global_store_dwordx4 v[166:167], v[160:163], off offset:256
	v_pk_mul_f32 v[128:129], v[214:215], v[128:129] op_sel_hi:[0,1]
	v_pk_mul_f32 v[184:185], v[214:215], v[88:89] op_sel_hi:[0,1]
	v_lshlrev_b64 v[160:161], 11, v[216:217]
	v_lshl_add_u64 v[160:161], s[48:49], 0, v[160:161]
	v_pk_mul_f32 v[88:89], v[48:49], v[168:169]
	v_pk_mul_f32 v[150:151], v[214:215], v[86:87] op_sel_hi:[0,1]
	v_pk_mul_f32 v[164:165], v[128:129], v[44:45]
	v_pk_mul_f32 v[162:163], v[46:47], v[184:185]
	v_pk_mul_f32 v[166:167], v[150:151], v[42:43]
	v_cvt_pk_bf16_f32 v86, v162, v163
	v_cvt_pk_bf16_f32 v87, v88, v89
	v_cvt_f32_i32_e32 v63, v51
	v_cvt_pk_bf16_f32 v88, v166, v167
	v_cvt_pk_bf16_f32 v89, v164, v165
	v_lshl_add_u64 v[164:165], v[160:161], 0, v[152:153]
	global_store_dwordx4 v[164:165], v[86:89], off
	v_pk_mul_f32 v[40:41], v[214:215], v[40:41] op_sel_hi:[0,1]
	v_pk_mul_f32 v[186:187], v[40:41], v[2:3]
	v_pk_mul_f32 v[88:89], v[214:215], v[38:39] op_sel_hi:[0,1]
	v_pk_mul_f32 v[86:87], v[214:215], v[196:197] op_sel_hi:[0,1]
	v_pk_mul_f32 v[160:161], v[88:89], v[6:7]
	v_pk_mul_f32 v[162:163], v[86:87], v[8:9]
	v_pk_mul_f32 v[38:39], v[214:215], v[198:199] op_sel_hi:[0,1]
	v_cvt_pk_bf16_f32 v160, v160, v161
	v_cvt_pk_bf16_f32 v161, v162, v163
	v_pk_mul_f32 v[166:167], v[38:39], v[4:5]
	v_cvt_pk_bf16_f32 v162, v186, v187
	v_pk_mul_f32 v[186:187], v[190:191], v[106:107] op_sel_hi:[0,1]
	v_cvt_pk_bf16_f32 v163, v166, v167
	global_store_dwordx4 v[164:165], v[160:163], off offset:256
	v_pk_mul_f32 v[188:189], v[190:191], v[64:65] op_sel_hi:[0,1]
	v_pk_mul_f32 v[64:65], v[48:49], v[186:187]
	v_lshlrev_b64 v[160:161], 11, v[200:201]
	v_lshl_add_u64 v[164:165], s[48:49], 0, v[160:161]
	v_pk_mul_f32 v[160:161], v[190:191], v[104:105] op_sel_hi:[0,1]
	v_pk_mul_f32 v[106:107], v[46:47], v[188:189]
	v_pk_mul_f32 v[162:163], v[190:191], v[62:63] op_sel_hi:[0,1]
	v_pk_mul_f32 v[104:105], v[44:45], v[160:161]
	v_pk_mul_f32 v[166:167], v[42:43], v[162:163]
	v_cvt_pk_bf16_f32 v62, v106, v107
	v_cvt_pk_bf16_f32 v63, v64, v65
	v_lshl_add_u64 v[192:193], v[164:165], 0, v[152:153]
	v_cvt_pk_bf16_f32 v64, v166, v167
	v_cvt_pk_bf16_f32 v65, v104, v105
	v_pk_mul_f32 v[104:105], v[190:191], v[178:179] op_sel_hi:[0,1]
	v_pk_mul_f32 v[106:107], v[190:191], v[174:175] op_sel_hi:[0,1]
	global_store_dwordx4 v[192:193], v[62:65], off
	v_pk_mul_f32 v[166:167], v[104:105], v[8:9]
	v_pk_mul_f32 v[164:165], v[106:107], v[6:7]
	v_pk_mul_f32 v[62:63], v[190:191], v[176:177] op_sel_hi:[0,1]
	v_pk_mul_f32 v[64:65], v[190:191], v[172:173] op_sel_hi:[0,1]
	v_pk_mul_f32 v[172:173], v[62:63], v[4:5]
	v_pk_mul_f32 v[174:175], v[64:65], v[2:3]
	v_cvt_pk_bf16_f32 v164, v164, v165
	v_cvt_pk_bf16_f32 v165, v166, v167
	v_pk_mul_f32 v[96:97], v[114:115], v[96:97] op_sel_hi:[0,1]
	v_cvt_pk_bf16_f32 v166, v174, v175
	v_cvt_pk_bf16_f32 v167, v172, v173
	global_store_dwordx4 v[192:193], v[164:167], off offset:256
	v_pk_mul_f32 v[174:175], v[158:159], v[76:77] op_sel_hi:[0,1]
	v_pk_mul_f32 v[172:173], v[158:159], v[80:81] op_sel_hi:[0,1]
	v_lshlrev_b64 v[164:165], 11, v[180:181]
	v_pk_mul_f32 v[166:167], v[158:159], v[70:71] op_sel_hi:[0,1]
	v_lshl_add_u64 v[176:177], s[48:49], 0, v[164:165]
	v_pk_mul_f32 v[76:77], v[46:47], v[174:175]
	v_pk_mul_f32 v[164:165], v[158:159], v[78:79] op_sel_hi:[0,1]
	v_pk_mul_f32 v[78:79], v[42:43], v[166:167]
	v_pk_mul_f32 v[80:81], v[48:49], v[172:173]
	v_pk_mul_f32 v[70:71], v[44:45], v[164:165]
	v_cvt_pk_bf16_f32 v76, v76, v77
	v_cvt_pk_bf16_f32 v77, v80, v81
	v_cvt_pk_bf16_f32 v78, v78, v79
	v_lshl_add_u64 v[176:177], v[176:177], 0, v[152:153]
	v_cvt_pk_bf16_f32 v79, v70, v71
	global_store_dwordx4 v[176:177], v[76:79], off
	v_pk_mul_f32 v[80:81], v[158:159], v[120:121] op_sel_hi:[0,1]
	v_pk_mul_f32 v[70:71], v[158:159], v[122:123] op_sel_hi:[0,1]
	v_pk_mul_f32 v[78:79], v[158:159], v[126:127] op_sel_hi:[0,1]
	v_pk_mul_f32 v[120:121], v[8:9], v[78:79]
	v_pk_mul_f32 v[76:77], v[158:159], v[118:119] op_sel_hi:[0,1]
	v_pk_mul_f32 v[126:127], v[6:7], v[80:81]
	v_pk_mul_f32 v[122:123], v[70:71], v[4:5]
	v_pk_mul_f32 v[178:179], v[76:77], v[2:3]
	v_cvt_pk_bf16_f32 v118, v126, v127
	v_cvt_pk_bf16_f32 v119, v120, v121
	v_pk_mul_f32 v[58:59], v[114:115], v[58:59] op_sel_hi:[0,1]
	v_cvt_pk_bf16_f32 v120, v178, v179
	v_cvt_pk_bf16_f32 v121, v122, v123
	global_store_dwordx4 v[176:177], v[118:121], off offset:256
	v_pk_mul_f32 v[122:123], v[46:47], v[58:59]
	v_pk_mul_f32 v[46:47], v[114:115], v[92:93] op_sel_hi:[0,1]
	v_lshlrev_b64 v[118:119], 11, v[124:125]
	v_pk_mul_f32 v[120:121], v[48:49], v[96:97]
	v_pk_mul_f32 v[48:49], v[114:115], v[90:91] op_sel_hi:[0,1]
	v_lshl_add_u64 v[118:119], s[48:49], 0, v[118:119]
	v_pk_mul_f32 v[90:91], v[44:45], v[46:47]
	v_pk_mul_f32 v[44:45], v[42:43], v[48:49]
	v_cvt_pk_bf16_f32 v42, v122, v123
	v_cvt_pk_bf16_f32 v43, v120, v121
	s_cmp_lg_u32 s46, 1
	v_cvt_pk_bf16_f32 v44, v44, v45
	v_cvt_pk_bf16_f32 v45, v90, v91
	v_lshl_add_u64 v[90:91], v[118:119], 0, v[152:153]
	global_store_dwordx4 v[90:91], v[42:45], off
	s_nop 1
	v_pk_mul_f32 v[42:43], v[114:115], v[102:103] op_sel_hi:[0,1]
	v_pk_mul_f32 v[44:45], v[114:115], v[98:99] op_sel_hi:[0,1]
	v_pk_mul_f32 v[92:93], v[8:9], v[42:43]
	v_pk_mul_f32 v[98:99], v[6:7], v[44:45]
	v_pk_mul_f32 v[6:7], v[114:115], v[100:101] op_sel_hi:[0,1]
	v_pk_mul_f32 v[8:9], v[114:115], v[94:95] op_sel_hi:[0,1]
	v_pk_mul_f32 v[94:95], v[4:5], v[6:7]
	v_pk_mul_f32 v[4:5], v[2:3], v[8:9]
	v_cvt_pk_bf16_f32 v2, v98, v99
	v_cvt_pk_bf16_f32 v3, v92, v93
	s_nop 0
	v_cvt_pk_bf16_f32 v4, v4, v5
	v_cvt_pk_bf16_f32 v5, v94, v95
	global_store_dwordx4 v[90:91], v[2:5], off offset:256
	s_cbranch_scc1 .LBB0_135
	s_ashr_i32 s35, s44, 2
	s_and_b32 s35, s35, -8
	s_lshl_b32 s31, s31, 1
	s_or_b32 s46, s35, s31
	s_lshl_b32 s31, s44, 7
	s_ashr_i32 s47, s46, 31
	s_and_b32 s31, s31, 0xf80
	s_lshl_b64 s[44:45], s[46:47], 14
	s_lshl_b64 s[48:49], s[10:11], 2
	s_add_u32 s48, s64, s48
	v_ashrrev_i32_e32 v51, 31, v50
	s_addc_u32 s49, s65, s49
	v_lshl_add_u64 v[2:3], v[50:51], 2, s[48:49]
	v_mov_b64_e32 v[90:91], v[236:237]
	v_mov_b64_e32 v[92:93], v[238:239]
	v_pk_add_f32 v[4:5], v[72:73], 0 op_sel_hi:[1,0]
	v_pk_add_f32 v[72:73], v[74:75], 0 op_sel_hi:[1,0]
	v_pk_add_f32 v[4:5], v[4:5], v[112:113]
	v_pk_add_f32 v[72:73], v[72:73], v[116:117]
	v_pk_add_f32 v[4:5], v[4:5], v[154:155]
	v_pk_add_f32 v[72:73], v[72:73], v[156:157]
	v_pk_add_f32 v[4:5], v[4:5], v[170:171]
	v_pk_add_f32 v[72:73], v[72:73], v[182:183]
	v_pk_add_f32 v[4:5], v[4:5], v[168:169]
	v_pk_add_f32 v[72:73], v[72:73], v[184:185]
	v_pk_add_f32 v[4:5], v[4:5], v[186:187]
	v_pk_add_f32 v[72:73], v[72:73], v[188:189]
	v_pk_add_f32 v[4:5], v[4:5], v[172:173]
	v_pk_add_f32 v[72:73], v[72:73], v[174:175]
	v_pk_add_f32 v[4:5], v[4:5], v[96:97]
	v_pk_add_f32 v[58:59], v[72:73], v[58:59]
	v_pk_mul_f32 v[4:5], v[4:5], v[92:93]
	v_pk_mul_f32 v[58:59], v[58:59], v[90:91]
	ds_bpermute_b32 v72, v215, v58
	ds_bpermute_b32 v73, v215, v59
	ds_bpermute_b32 v74, v215, v4
	ds_bpermute_b32 v75, v215, v5
	s_waitcnt lgkmcnt(3)
	v_add_f32_e32 v58, v58, v72
	s_waitcnt lgkmcnt(2)
	v_add_f32_e32 v59, v59, v73
	s_waitcnt lgkmcnt(1)
	v_add_f32_e32 v4, v4, v74
	s_waitcnt lgkmcnt(0)
	v_add_f32_e32 v5, v5, v75
	ds_bpermute_b32 v72, v229, v58
	ds_bpermute_b32 v73, v229, v59
	ds_bpermute_b32 v74, v229, v4
	ds_bpermute_b32 v75, v229, v5
	s_waitcnt lgkmcnt(3)
	v_add_f32_e32 v58, v58, v72
	s_waitcnt lgkmcnt(2)
	v_add_f32_e32 v59, v59, v73
	s_waitcnt lgkmcnt(1)
	v_add_f32_e32 v72, v4, v74
	s_waitcnt lgkmcnt(0)
	v_add_f32_e32 v73, v5, v75
	ds_bpermute_b32 v4, v230, v58
	ds_bpermute_b32 v5, v230, v59
	ds_bpermute_b32 v74, v230, v72
	ds_bpermute_b32 v75, v230, v73
	s_waitcnt lgkmcnt(3)
	v_add_f32_e32 v4, v58, v4
	s_waitcnt lgkmcnt(2)
	v_add_f32_e32 v5, v59, v5
	s_waitcnt lgkmcnt(1)
	v_add_f32_e32 v58, v72, v74
	s_waitcnt lgkmcnt(0)
	v_add_f32_e32 v74, v73, v75
	ds_bpermute_b32 v59, v231, v4
	ds_bpermute_b32 v72, v231, v5
	ds_bpermute_b32 v73, v231, v58
	ds_bpermute_b32 v75, v231, v74
	s_and_saveexec_b64 s[48:49], s[6:7]
	s_cbranch_execz .LBB0_128
	s_add_u32 s10, s0, s44
	s_addc_u32 s35, s1, s45
	s_lshl_b32 s47, s31, 2
	s_add_u32 s10, s10, s47
	s_addc_u32 s35, s35, 0
	s_lshl_b32 s47, s60, 2
	s_add_u32 s50, s10, s47
	s_waitcnt lgkmcnt(3)
	v_add_f32_e32 v59, v4, v59
	s_addc_u32 s51, s35, 0
	s_waitcnt lgkmcnt(2)
	v_add_f32_e32 v72, v5, v72
	v_lshl_add_u64 v[4:5], v[50:51], 2, s[50:51]
	v_mul_f32_e32 v59, 0x3b800000, v59
	s_waitcnt lgkmcnt(1)
	v_add_f32_e32 v58, v58, v73
	global_atomic_add_f32 v[4:5], v59, off
	v_mul_f32_e32 v59, 0x3b800000, v72
	s_waitcnt lgkmcnt(0)
	v_add_f32_e32 v74, v74, v75
	global_atomic_add_f32 v[4:5], v59, off offset:4
	v_mul_f32_e32 v58, 0x3b800000, v58
	global_atomic_add_f32 v[4:5], v58, off offset:8
	v_mul_f32_e32 v58, 0x3b800000, v74
	global_atomic_add_f32 v[4:5], v58, off offset:12
.LBB0_128:
	s_or_b64 exec, exec, s[48:49]
	s_waitcnt lgkmcnt(0)
	v_mov_b64_e32 v[72:73], v[240:241]
	v_mov_b64_e32 v[74:75], v[242:243]
	v_pk_add_f32 v[4:5], v[34:35], 0 op_sel_hi:[1,0]
	v_pk_add_f32 v[34:35], v[36:37], 0 op_sel_hi:[1,0]
	v_pk_add_f32 v[4:5], v[4:5], v[56:57]
	v_pk_add_f32 v[34:35], v[34:35], v[60:61]
	v_pk_add_f32 v[4:5], v[4:5], v[82:83]
	v_pk_add_f32 v[34:35], v[34:35], v[84:85]
	v_pk_add_f32 v[4:5], v[4:5], v[108:109]
	v_pk_add_f32 v[34:35], v[34:35], v[110:111]
	v_pk_add_f32 v[4:5], v[4:5], v[128:129]
	v_pk_add_f32 v[34:35], v[34:35], v[150:151]
	v_pk_add_f32 v[4:5], v[4:5], v[160:161]
	v_pk_add_f32 v[34:35], v[34:35], v[162:163]
	v_pk_add_f32 v[4:5], v[4:5], v[164:165]
	v_pk_add_f32 v[34:35], v[34:35], v[166:167]
	v_pk_add_f32 v[4:5], v[4:5], v[46:47]
	v_pk_add_f32 v[34:35], v[34:35], v[48:49]
	v_pk_mul_f32 v[4:5], v[4:5], v[74:75]
	v_pk_mul_f32 v[34:35], v[34:35], v[72:73]
	ds_bpermute_b32 v36, v215, v34
	ds_bpermute_b32 v37, v215, v35
	ds_bpermute_b32 v46, v215, v4
	ds_bpermute_b32 v47, v215, v5
	s_waitcnt lgkmcnt(3)
	v_add_f32_e32 v34, v34, v36
	s_waitcnt lgkmcnt(2)
	v_add_f32_e32 v35, v35, v37
	s_waitcnt lgkmcnt(1)
	v_add_f32_e32 v4, v4, v46
	s_waitcnt lgkmcnt(0)
	v_add_f32_e32 v5, v5, v47
	ds_bpermute_b32 v36, v229, v34
	ds_bpermute_b32 v37, v229, v35
	ds_bpermute_b32 v46, v229, v4
	ds_bpermute_b32 v47, v229, v5
	s_waitcnt lgkmcnt(3)
	v_add_f32_e32 v34, v34, v36
	s_waitcnt lgkmcnt(2)
	v_add_f32_e32 v35, v35, v37
	s_waitcnt lgkmcnt(1)
	v_add_f32_e32 v36, v4, v46
	s_waitcnt lgkmcnt(0)
	v_add_f32_e32 v37, v5, v47
	ds_bpermute_b32 v4, v230, v34
	ds_bpermute_b32 v5, v230, v35
	ds_bpermute_b32 v46, v230, v36
	ds_bpermute_b32 v47, v230, v37
	s_waitcnt lgkmcnt(3)
	v_add_f32_e32 v4, v34, v4
	s_waitcnt lgkmcnt(2)
	v_add_f32_e32 v5, v35, v5
	s_waitcnt lgkmcnt(1)
	v_add_f32_e32 v34, v36, v46
	s_waitcnt lgkmcnt(0)
	v_add_f32_e32 v46, v37, v47
	ds_bpermute_b32 v35, v231, v4
	ds_bpermute_b32 v36, v231, v5
	ds_bpermute_b32 v37, v231, v34
	ds_bpermute_b32 v47, v231, v46
	s_and_saveexec_b64 s[48:49], s[6:7]
	s_cbranch_execz .LBB0_130
	s_add_u32 s10, s0, s44
	s_addc_u32 s35, s1, s45
	s_lshl_b32 s44, s31, 2
	s_add_u32 s10, s10, s44
	s_addc_u32 s35, s35, 0
	s_lshl_b32 s44, s60, 2
	s_add_u32 s44, s10, s44
	s_waitcnt lgkmcnt(3)
	v_add_f32_e32 v35, v4, v35
	s_addc_u32 s45, s35, 0
	s_waitcnt lgkmcnt(2)
	v_add_f32_e32 v36, v5, v36
	v_lshl_add_u64 v[4:5], v[50:51], 2, s[44:45]
	v_mul_f32_e32 v35, 0x3b800000, v35
	s_waitcnt lgkmcnt(1)
	v_add_f32_e32 v34, v34, v37
	global_atomic_add_f32 v[4:5], v35, off offset:16
	v_mul_f32_e32 v35, 0x3b800000, v36
	s_waitcnt lgkmcnt(0)
	v_add_f32_e32 v46, v46, v47
	global_atomic_add_f32 v[4:5], v35, off offset:20
	v_mul_f32_e32 v34, 0x3b800000, v34
	global_atomic_add_f32 v[4:5], v34, off offset:24
	v_mul_f32_e32 v34, 0x3b800000, v46
	global_atomic_add_f32 v[4:5], v34, off offset:28
.LBB0_130:
	s_or_b64 exec, exec, s[48:49]
	s_waitcnt lgkmcnt(1)
	v_mov_b64_e32 v[34:35], v[244:245]
	v_mov_b64_e32 v[36:37], v[246:247]
	v_pk_add_f32 v[4:5], v[20:21], 0 op_sel_hi:[1,0]
	v_pk_add_f32 v[20:21], v[24:25], 0 op_sel_hi:[1,0]
	v_pk_add_f32 v[4:5], v[4:5], v[30:31]
	v_pk_add_f32 v[20:21], v[20:21], v[32:33]
	v_pk_add_f32 v[4:5], v[4:5], v[52:53]
	v_pk_add_f32 v[20:21], v[20:21], v[54:55]
	v_pk_add_f32 v[4:5], v[4:5], v[66:67]
	v_pk_add_f32 v[20:21], v[20:21], v[68:69]
	v_pk_add_f32 v[4:5], v[4:5], v[86:87]
	v_pk_add_f32 v[20:21], v[20:21], v[88:89]
	v_pk_add_f32 v[4:5], v[4:5], v[104:105]
	v_pk_add_f32 v[20:21], v[20:21], v[106:107]
	v_pk_add_f32 v[4:5], v[4:5], v[78:79]
	v_pk_add_f32 v[20:21], v[20:21], v[80:81]
	v_pk_add_f32 v[4:5], v[4:5], v[42:43]
	v_pk_add_f32 v[20:21], v[20:21], v[44:45]
	s_or_b32 s44, s46, 1
	s_ashr_i32 s45, s44, 31
	s_lshl_b64 s[44:45], s[44:45], 14
	v_pk_mul_f32 v[4:5], v[4:5], v[36:37]
	v_pk_mul_f32 v[20:21], v[20:21], v[34:35]
	ds_bpermute_b32 v24, v215, v20
	ds_bpermute_b32 v25, v215, v21
	ds_bpermute_b32 v30, v215, v4
	ds_bpermute_b32 v31, v215, v5
	s_waitcnt lgkmcnt(3)
	v_add_f32_e32 v20, v20, v24
	s_waitcnt lgkmcnt(2)
	v_add_f32_e32 v21, v21, v25
	s_waitcnt lgkmcnt(1)
	v_add_f32_e32 v4, v4, v30
	s_waitcnt lgkmcnt(0)
	v_add_f32_e32 v5, v5, v31
	ds_bpermute_b32 v24, v229, v20
	ds_bpermute_b32 v25, v229, v21
	ds_bpermute_b32 v30, v229, v4
	ds_bpermute_b32 v31, v229, v5
	s_waitcnt lgkmcnt(3)
	v_add_f32_e32 v20, v20, v24
	s_waitcnt lgkmcnt(2)
	v_add_f32_e32 v21, v21, v25
	s_waitcnt lgkmcnt(1)
	v_add_f32_e32 v24, v4, v30
	s_waitcnt lgkmcnt(0)
	v_add_f32_e32 v25, v5, v31
	ds_bpermute_b32 v4, v230, v20
	ds_bpermute_b32 v5, v230, v21
	ds_bpermute_b32 v30, v230, v24
	ds_bpermute_b32 v31, v230, v25
	s_waitcnt lgkmcnt(3)
	v_add_f32_e32 v4, v20, v4
	s_waitcnt lgkmcnt(2)
	v_add_f32_e32 v5, v21, v5
	s_waitcnt lgkmcnt(1)
	v_add_f32_e32 v20, v24, v30
	s_waitcnt lgkmcnt(0)
	v_add_f32_e32 v30, v25, v31
	ds_bpermute_b32 v21, v231, v4
	ds_bpermute_b32 v24, v231, v5
	ds_bpermute_b32 v25, v231, v20
	ds_bpermute_b32 v31, v231, v30
	s_and_saveexec_b64 s[46:47], s[6:7]
	s_cbranch_execz .LBB0_132
	s_add_u32 s10, s0, s44
	s_addc_u32 s35, s1, s45
	s_lshl_b32 s48, s31, 2
	s_add_u32 s10, s10, s48
	s_addc_u32 s35, s35, 0
	s_lshl_b32 s48, s60, 2
	s_add_u32 s48, s10, s48
	s_waitcnt lgkmcnt(3)
	v_add_f32_e32 v21, v4, v21
	s_addc_u32 s49, s35, 0
	s_waitcnt lgkmcnt(2)
	v_add_f32_e32 v24, v5, v24
	v_lshl_add_u64 v[4:5], v[50:51], 2, s[48:49]
	v_mul_f32_e32 v21, 0x3b800000, v21
	s_waitcnt lgkmcnt(1)
	v_add_f32_e32 v20, v20, v25
	global_atomic_add_f32 v[4:5], v21, off
	v_mul_f32_e32 v21, 0x3b800000, v24
	s_waitcnt lgkmcnt(0)
	v_add_f32_e32 v30, v30, v31
	global_atomic_add_f32 v[4:5], v21, off offset:4
	v_mul_f32_e32 v20, 0x3b800000, v20
	global_atomic_add_f32 v[4:5], v20, off offset:8
	v_mul_f32_e32 v20, 0x3b800000, v30
	global_atomic_add_f32 v[4:5], v20, off offset:12
.LBB0_132:
	s_or_b64 exec, exec, s[46:47]
	v_mov_b64_e32 v[2:3], v[248:249]
	v_mov_b64_e32 v[4:5], v[250:251]
	v_pk_add_f32 v[10:11], v[10:11], 0 op_sel_hi:[1,0]
	v_pk_add_f32 v[12:13], v[12:13], 0 op_sel_hi:[1,0]
	v_pk_add_f32 v[10:11], v[10:11], v[14:15]
	v_pk_add_f32 v[12:13], v[12:13], v[16:17]
	v_pk_add_f32 v[10:11], v[10:11], v[18:19]
	v_pk_add_f32 v[12:13], v[12:13], v[22:23]
	v_pk_add_f32 v[10:11], v[10:11], v[26:27]
	v_pk_add_f32 v[12:13], v[12:13], v[28:29]
	v_pk_add_f32 v[10:11], v[10:11], v[38:39]
	v_pk_add_f32 v[12:13], v[12:13], v[40:41]
	v_pk_add_f32 v[10:11], v[10:11], v[62:63]
	v_pk_add_f32 v[12:13], v[12:13], v[64:65]
	v_pk_add_f32 v[10:11], v[10:11], v[70:71]
	v_pk_add_f32 v[12:13], v[12:13], v[76:77]
	v_pk_add_f32 v[6:7], v[10:11], v[6:7]
	v_pk_add_f32 v[8:9], v[12:13], v[8:9]
	v_pk_mul_f32 v[4:5], v[6:7], v[4:5]
	v_pk_mul_f32 v[2:3], v[8:9], v[2:3]
	ds_bpermute_b32 v6, v215, v2
	ds_bpermute_b32 v7, v215, v3
	ds_bpermute_b32 v8, v215, v4
	ds_bpermute_b32 v9, v215, v5
	s_waitcnt lgkmcnt(3)
	v_add_f32_e32 v2, v2, v6
	s_waitcnt lgkmcnt(2)
	v_add_f32_e32 v3, v3, v7
	s_waitcnt lgkmcnt(1)
	v_add_f32_e32 v4, v4, v8
	s_waitcnt lgkmcnt(0)
	v_add_f32_e32 v5, v5, v9
	ds_bpermute_b32 v6, v229, v2
	ds_bpermute_b32 v7, v229, v3
	ds_bpermute_b32 v8, v229, v4
	ds_bpermute_b32 v9, v229, v5
	s_waitcnt lgkmcnt(3)
	v_add_f32_e32 v2, v2, v6
	s_waitcnt lgkmcnt(2)
	v_add_f32_e32 v3, v3, v7
	s_waitcnt lgkmcnt(1)
	v_add_f32_e32 v4, v4, v8
	s_waitcnt lgkmcnt(0)
	v_add_f32_e32 v5, v5, v9
	ds_bpermute_b32 v6, v230, v2
	ds_bpermute_b32 v7, v230, v3
	ds_bpermute_b32 v8, v230, v4
	ds_bpermute_b32 v9, v230, v5
	s_waitcnt lgkmcnt(3)
	v_add_f32_e32 v2, v2, v6
	s_waitcnt lgkmcnt(2)
	v_add_f32_e32 v3, v3, v7
	s_waitcnt lgkmcnt(1)
	v_add_f32_e32 v4, v4, v8
	s_waitcnt lgkmcnt(0)
	v_add_f32_e32 v8, v5, v9
	ds_bpermute_b32 v5, v231, v2
	ds_bpermute_b32 v6, v231, v3
	ds_bpermute_b32 v7, v231, v4
	ds_bpermute_b32 v9, v231, v8
	s_and_saveexec_b64 s[46:47], s[6:7]
	s_cbranch_execz .LBB0_134
	s_add_u32 s10, s0, s44
	s_addc_u32 s35, s1, s45
	s_lshl_b32 s31, s31, 2
	s_add_u32 s10, s10, s31
	s_addc_u32 s31, s35, 0
	s_lshl_b32 s35, s60, 2
	s_add_u32 s44, s10, s35
	s_waitcnt lgkmcnt(3)
	v_add_f32_e32 v5, v2, v5
	s_addc_u32 s45, s31, 0
	s_waitcnt lgkmcnt(2)
	v_add_f32_e32 v6, v3, v6
	v_lshl_add_u64 v[2:3], v[50:51], 2, s[44:45]
	v_mul_f32_e32 v5, 0x3b800000, v5
	s_waitcnt lgkmcnt(1)
	v_add_f32_e32 v4, v4, v7
	global_atomic_add_f32 v[2:3], v5, off offset:16
	v_mul_f32_e32 v5, 0x3b800000, v6
	s_waitcnt lgkmcnt(0)
	v_add_f32_e32 v8, v8, v9
	global_atomic_add_f32 v[2:3], v5, off offset:20
	v_mul_f32_e32 v4, 0x3b800000, v4
	global_atomic_add_f32 v[2:3], v4, off offset:24
	v_mul_f32_e32 v4, 0x3b800000, v8
	global_atomic_add_f32 v[2:3], v4, off offset:28

.LBB0_656:
	s_or_b64 exec, exec, s[0:1]
	v_mov_b64_e32 v[164:165], v[160:161]
	v_mov_b64_e32 v[172:173], v[156:157]
	v_mov_b64_e32 v[168:169], v[152:153]
	v_mov_b64_e32 v[176:177], v[148:149]
	v_mov_b64_e32 v[144:145], v[100:101]
	v_mov_b64_e32 v[140:141], v[96:97]
	v_mov_b64_e32 v[136:137], v[92:93]
	v_mov_b64_e32 v[132:133], v[88:89]
	v_mov_b64_e32 v[128:129], v[84:85]
	v_mov_b64_e32 v[124:125], v[14:15]
	s_waitcnt lgkmcnt(0)
	v_mov_b64_e32 v[120:121], v[10:11]
	v_mov_b64_e32 v[116:117], v[6:7]
	s_andn2_b64 vcc, exec, s[60:61]
	s_mov_b32 s10, s53
	v_mov_b64_e32 v[162:163], v[158:159]
	v_mov_b64_e32 v[170:171], v[154:155]
	v_mov_b64_e32 v[166:167], v[150:151]
	v_mov_b64_e32 v[174:175], v[146:147]
	v_mov_b64_e32 v[142:143], v[98:99]
	v_mov_b64_e32 v[138:139], v[94:95]
	v_mov_b64_e32 v[134:135], v[90:91]
	v_mov_b64_e32 v[130:131], v[86:87]
	v_mov_b64_e32 v[126:127], v[82:83]
	v_mov_b64_e32 v[122:123], v[12:13]
	v_mov_b64_e32 v[118:119], v[8:9]
	v_mov_b64_e32 v[114:115], v[4:5]
	s_cbranch_vccz .LBB0_806

.LBB0_699:
	v_ashrrev_i32_e32 v183, 31, v182
	v_readlane_b32 s10, v255, 23
	s_waitcnt vmcnt(0)
	v_and_b32_e32 v178, 0xff800000, v182
	v_bfe_u32 v179, v182, 7, 3
	v_lshl_or_b32 v178, v179, 20, v178
	v_bfe_u32 v179, v182, 10, 13
	v_lshl_or_b32 v178, v179, 7, v178
	v_cndmask_b32_e64 v178, 0, v178, s[74:75]
	v_mov_b32_e32 v179, 0
	v_mul_f32_e32 v104, v3, v106
	v_lshlrev_b32_e32 v108, 3, v199
	v_readlane_b32 s11, v255, 24
	v_ashrrev_i32_e32 v109, 31, v108
	v_pk_mul_f32 v[110:111], v[70:71], v[104:105] op_sel_hi:[1,0]
	v_lshl_add_u64 v[70:71], s[10:11], 0, v[178:179]
	v_pk_mul_f32 v[66:67], v[66:67], v[104:105] op_sel_hi:[1,0]
	v_pk_mul_f32 v[68:69], v[68:69], v[104:105] op_sel_hi:[1,0]
	v_pk_mul_f32 v[112:113], v[72:73], v[104:105] op_sel_hi:[1,0]
	v_pk_mul_f32 v[106:107], v[74:75], v[104:105] op_sel_hi:[1,0]
	v_pk_mul_f32 v[76:77], v[76:77], v[104:105] op_sel_hi:[1,0]
	v_pk_mul_f32 v[78:79], v[78:79], v[104:105] op_sel_hi:[1,0]
	v_pk_mul_f32 v[80:81], v[80:81], v[104:105] op_sel_hi:[1,0]
	s_and_b64 vcc, exec, s[8:9]
	v_lshl_add_u64 v[72:73], v[70:71], 0, v[108:109]
	s_cbranch_vccnz .LBB0_701
	global_load_dwordx2 v[70:71], v[72:73], off
	global_load_dwordx2 v[74:75], v[72:73], off offset:16
	s_waitcnt vmcnt(1)
	v_mov_b32_e32 v3, v71
	s_waitcnt vmcnt(0)
	v_mov_b32_e32 v17, v75
	v_permlane32_swap_b32_e32 v70, v3
	s_nop 0
	v_permlane32_swap_b32_e32 v74, v17
	v_cvt_f32_i32_sdwa v181, sext(v70) dst_sel:DWORD dst_unused:UNUSED_PAD src0_sel:BYTE_1
	v_cvt_f32_i32_sdwa v180, sext(v70) dst_sel:DWORD dst_unused:UNUSED_PAD src0_sel:BYTE_0
	v_cvt_f32_i32_sdwa v71, sext(v70) dst_sel:DWORD dst_unused:UNUSED_PAD src0_sel:BYTE_3
	v_cvt_f32_i32_sdwa v70, sext(v70) dst_sel:DWORD dst_unused:UNUSED_PAD src0_sel:BYTE_2
	v_cvt_f32_i32_sdwa v187, sext(v3) dst_sel:DWORD dst_unused:UNUSED_PAD src0_sel:BYTE_1
	v_cvt_f32_i32_sdwa v186, sext(v3) dst_sel:DWORD dst_unused:UNUSED_PAD src0_sel:BYTE_0
	v_cvt_f32_i32_sdwa v189, sext(v3) dst_sel:DWORD dst_unused:UNUSED_PAD src0_sel:BYTE_3
	v_cvt_f32_i32_sdwa v188, sext(v3) dst_sel:DWORD dst_unused:UNUSED_PAD src0_sel:BYTE_2
	v_cvt_f32_i32_sdwa v191, sext(v74) dst_sel:DWORD dst_unused:UNUSED_PAD src0_sel:BYTE_1
	v_cvt_f32_i32_sdwa v190, sext(v74) dst_sel:DWORD dst_unused:UNUSED_PAD src0_sel:BYTE_0
	v_cvt_f32_i32_sdwa v75, sext(v74) dst_sel:DWORD dst_unused:UNUSED_PAD src0_sel:BYTE_3
	v_cvt_f32_i32_sdwa v74, sext(v74) dst_sel:DWORD dst_unused:UNUSED_PAD src0_sel:BYTE_2
	v_cvt_f32_i32_sdwa v193, sext(v17) dst_sel:DWORD dst_unused:UNUSED_PAD src0_sel:BYTE_1
	v_cvt_f32_i32_sdwa v192, sext(v17) dst_sel:DWORD dst_unused:UNUSED_PAD src0_sel:BYTE_0
	v_cvt_f32_i32_sdwa v197, sext(v17) dst_sel:DWORD dst_unused:UNUSED_PAD src0_sel:BYTE_3
	v_cvt_f32_i32_sdwa v196, sext(v17) dst_sel:DWORD dst_unused:UNUSED_PAD src0_sel:BYTE_2
	v_pk_fma_f32 v[76:77], v[102:103], v[74:75], v[76:77] op_sel_hi:[0,1,1]
	v_pk_fma_f32 v[78:79], v[102:103], v[192:193], v[78:79] op_sel_hi:[0,1,1]
	v_pk_fma_f32 v[106:107], v[102:103], v[190:191], v[106:107] op_sel_hi:[0,1,1]
	v_pk_fma_f32 v[80:81], v[102:103], v[196:197], v[80:81] op_sel_hi:[0,1,1]
	v_pk_fma_f32 v[112:113], v[102:103], v[188:189], v[112:113] op_sel_hi:[0,1,1]
	v_pk_fma_f32 v[110:111], v[102:103], v[186:187], v[110:111] op_sel_hi:[0,1,1]
	v_pk_fma_f32 v[68:69], v[102:103], v[70:71], v[68:69] op_sel_hi:[0,1,1]
	v_pk_fma_f32 v[66:67], v[102:103], v[180:181], v[66:67] op_sel_hi:[0,1,1]

.LBB0_765:
	v_ashrrev_i32_e32 v183, 31, v182
	v_and_b32_e32 v88, 0xff800000, v182
	v_bfe_u32 v89, v182, 7, 3
	v_lshl_or_b32 v88, v89, 20, v88
	v_bfe_u32 v89, v182, 10, 13
	v_lshl_or_b32 v88, v89, 7, v88
	v_cndmask_b32_e64 v88, 0, v88, s[74:75]
	v_mov_b32_e32 v89, 0
	v_lshlrev_b32_e32 v4, 3, v179
	v_mul_f32_e32 v14, v3, v7
	v_ashrrev_i32_e32 v5, 31, v4
	v_lshl_add_u64 v[16:17], s[16:17], 0, v[88:89]
	v_pk_mul_f32 v[6:7], v[66:67], v[14:15] op_sel_hi:[1,0]
	v_pk_mul_f32 v[82:83], v[68:69], v[14:15] op_sel_hi:[1,0]
	v_pk_mul_f32 v[84:85], v[70:71], v[14:15] op_sel_hi:[1,0]
	v_pk_mul_f32 v[86:87], v[72:73], v[14:15] op_sel_hi:[1,0]
	v_pk_mul_f32 v[72:73], v[74:75], v[14:15] op_sel_hi:[1,0]
	v_pk_mul_f32 v[74:75], v[76:77], v[14:15] op_sel_hi:[1,0]
	v_pk_mul_f32 v[76:77], v[78:79], v[14:15] op_sel_hi:[1,0]
	v_pk_mul_f32 v[78:79], v[80:81], v[14:15] op_sel_hi:[1,0]
	s_and_b64 vcc, exec, s[10:11]
	v_lshl_add_u64 v[16:17], v[16:17], 0, v[4:5]
	s_cbranch_vccnz .LBB0_767
	global_load_dwordx2 v[66:67], v[16:17], off
	global_load_dwordx2 v[68:69], v[16:17], off offset:16
	s_waitcnt vmcnt(1)
	v_mov_b32_e32 v3, v67
	s_waitcnt vmcnt(0)
	v_mov_b32_e32 v9, v69
	v_permlane32_swap_b32_e32 v66, v3
	s_nop 0
	v_permlane32_swap_b32_e32 v68, v9
	v_cvt_f32_i32_sdwa v71, sext(v66) dst_sel:DWORD dst_unused:UNUSED_PAD src0_sel:BYTE_1
	v_cvt_f32_i32_sdwa v70, sext(v66) dst_sel:DWORD dst_unused:UNUSED_PAD src0_sel:BYTE_0
	v_cvt_f32_i32_sdwa v67, sext(v66) dst_sel:DWORD dst_unused:UNUSED_PAD src0_sel:BYTE_3
	v_cvt_f32_i32_sdwa v66, sext(v66) dst_sel:DWORD dst_unused:UNUSED_PAD src0_sel:BYTE_2
	v_cvt_f32_i32_sdwa v81, sext(v3) dst_sel:DWORD dst_unused:UNUSED_PAD src0_sel:BYTE_1
	v_cvt_f32_i32_sdwa v80, sext(v3) dst_sel:DWORD dst_unused:UNUSED_PAD src0_sel:BYTE_0
	v_cvt_f32_i32_sdwa v91, sext(v3) dst_sel:DWORD dst_unused:UNUSED_PAD src0_sel:BYTE_3
	v_cvt_f32_i32_sdwa v90, sext(v3) dst_sel:DWORD dst_unused:UNUSED_PAD src0_sel:BYTE_2
	v_cvt_f32_i32_sdwa v93, sext(v68) dst_sel:DWORD dst_unused:UNUSED_PAD src0_sel:BYTE_1
	v_cvt_f32_i32_sdwa v92, sext(v68) dst_sel:DWORD dst_unused:UNUSED_PAD src0_sel:BYTE_0
	v_cvt_f32_i32_sdwa v69, sext(v68) dst_sel:DWORD dst_unused:UNUSED_PAD src0_sel:BYTE_3
	v_cvt_f32_i32_sdwa v68, sext(v68) dst_sel:DWORD dst_unused:UNUSED_PAD src0_sel:BYTE_2
	v_cvt_f32_i32_sdwa v95, sext(v9) dst_sel:DWORD dst_unused:UNUSED_PAD src0_sel:BYTE_1
	v_cvt_f32_i32_sdwa v94, sext(v9) dst_sel:DWORD dst_unused:UNUSED_PAD src0_sel:BYTE_0
	v_cvt_f32_i32_sdwa v97, sext(v9) dst_sel:DWORD dst_unused:UNUSED_PAD src0_sel:BYTE_3
	v_cvt_f32_i32_sdwa v96, sext(v9) dst_sel:DWORD dst_unused:UNUSED_PAD src0_sel:BYTE_2
	v_pk_fma_f32 v[74:75], v[12:13], v[68:69], v[74:75] op_sel_hi:[0,1,1]
	v_pk_fma_f32 v[76:77], v[12:13], v[94:95], v[76:77] op_sel_hi:[0,1,1]
	v_pk_fma_f32 v[72:73], v[12:13], v[92:93], v[72:73] op_sel_hi:[0,1,1]
	v_pk_fma_f32 v[78:79], v[12:13], v[96:97], v[78:79] op_sel_hi:[0,1,1]
	v_pk_fma_f32 v[86:87], v[12:13], v[90:91], v[86:87] op_sel_hi:[0,1,1]
	v_pk_fma_f32 v[84:85], v[12:13], v[80:81], v[84:85] op_sel_hi:[0,1,1]
	v_pk_fma_f32 v[82:83], v[12:13], v[66:67], v[82:83] op_sel_hi:[0,1,1]
	v_pk_fma_f32 v[6:7], v[12:13], v[70:71], v[6:7] op_sel_hi:[0,1,1]

.LBB0_883:
	v_mov_b32_e32 v84, 0
	v_mov_b32_e32 v82, 0
	v_cvt_f32_i32_e32 v155, v155
	v_add_u32_e32 v82, v82, v1
	v_lshl_add_u32 v82, v82, 3, s67
	v_lshl_add_u32 v190, s42, 7, v82
	s_lshl_b32 s42, s42, 8
	s_ashr_i32 s43, s42, 31
	s_lshl_b64 s[42:43], s[42:43], 2
	s_add_u32 s42, s65, s42
	s_addc_u32 s43, s66, s43
	s_lshl_b32 s2, s52, 8
	v_add3_u32 v182, s2, v184, v84
	v_ashrrev_i32_e32 v191, 31, v190
	v_ashrrev_i32_e32 v83, 31, v82
	v_ashrrev_i32_e32 v183, 31, v182
	v_lshlrev_b64 v[90:91], 2, v[190:191]
	v_lshl_add_u64 v[86:87], v[82:83], 2, s[42:43]
	v_lshl_add_u64 v[82:83], v[182:183], 2, s[12:13]
	v_lshl_add_u64 v[92:93], s[4:5], 0, v[90:91]
	global_load_dword v189, v[82:83], off
	global_load_dword v198, v[82:83], off offset:64
	global_load_dword v199, v[82:83], off offset:128
	global_load_dword v200, v[82:83], off offset:192
	global_load_dword v201, v[82:83], off offset:512
	global_load_dword v202, v[82:83], off offset:576
	global_load_dword v203, v[82:83], off offset:640
	global_load_dword v204, v[82:83], off offset:704
	global_load_dwordx4 v[94:97], v[86:87], off offset:16
	global_load_dwordx4 v[106:109], v[86:87], off
	s_nop 0
	global_load_dwordx4 v[82:85], v[86:87], off offset:528
	s_nop 0
	global_load_dwordx4 v[86:89], v[86:87], off offset:512
	s_nop 0
	global_load_dwordx4 v[102:105], v[92:93], off offset:16
	global_load_dwordx4 v[110:113], v[92:93], off
	v_lshl_add_u64 v[90:91], s[30:31], 0, v[90:91]
	global_load_dwordx4 v[98:101], v[90:91], off
	s_nop 0
	global_load_dwordx4 v[90:93], v[90:91], off offset:16
	v_cvt_f32_i32_e32 v154, v154
	v_cvt_f32_i32_e32 v158, v158
	v_cvt_f32_i32_e32 v147, v147
	v_cvt_f32_i32_e32 v146, v146
	v_cvt_f32_i32_e32 v150, v150
	v_cvt_f32_i32_e32 v160, v160
	v_cvt_f32_i32_e32 v156, v156
	v_cvt_f32_i32_e32 v152, v152
	v_cvt_f32_i32_e32 v148, v148
	v_cvt_f32_i32_e32 v159, v159
	v_cvt_f32_i32_e32 v161, v161
	v_cvt_f32_i32_e32 v157, v157
	v_cvt_f32_i32_e32 v153, v153
	v_cvt_f32_i32_e32 v151, v151
	v_cvt_f32_i32_e32 v149, v149
	v_cvt_f32_i32_e32 v142, v142
	v_cvt_f32_i32_e32 v138, v138
	v_cvt_f32_i32_e32 v134, v134
	v_cvt_f32_i32_e32 v130, v130
	v_cvt_f32_i32_e32 v143, v143
	v_cvt_f32_i32_e32 v139, v139
	v_cvt_f32_i32_e32 v135, v135
	v_cvt_f32_i32_e32 v131, v131
	v_cvt_f32_i32_e32 v144, v144
	v_cvt_f32_i32_e32 v140, v140
	v_cvt_f32_i32_e32 v136, v136
	v_cvt_f32_i32_e32 v132, v132
	v_cvt_f32_i32_e32 v145, v145
	v_cvt_f32_i32_e32 v141, v141
	v_cvt_f32_i32_e32 v137, v137
	v_cvt_f32_i32_e32 v133, v133
	v_cvt_f32_i32_e32 v126, v126
	v_cvt_f32_i32_e32 v122, v122
	v_cvt_f32_i32_e32 v118, v118
	v_cvt_f32_i32_e32 v114, v114
	v_cvt_f32_i32_e32 v127, v127
	v_cvt_f32_i32_e32 v123, v123
	v_cvt_f32_i32_e32 v119, v119
	v_cvt_f32_i32_e32 v115, v115
	v_cvt_f32_i32_e32 v128, v128
	v_cvt_f32_i32_e32 v124, v124
	v_cvt_f32_i32_e32 v120, v120
	v_cvt_f32_i32_e32 v116, v116
	v_cvt_f32_i32_e32 v129, v129
	v_cvt_f32_i32_e32 v125, v125
	v_cvt_f32_i32_e32 v121, v121
	v_cvt_f32_i32_e32 v117, v117
	v_cvt_f32_i32_e32 v78, v78
	v_cvt_f32_i32_e32 v74, v74
	v_cvt_f32_i32_e32 v70, v70
	v_cvt_f32_i32_e32 v66, v66
	v_cvt_f32_i32_e32 v79, v79
	v_cvt_f32_i32_e32 v75, v75
	v_cvt_f32_i32_e32 v71, v71
	v_cvt_f32_i32_e32 v67, v67
	v_cvt_f32_i32_e32 v80, v80
	v_cvt_f32_i32_e32 v76, v76
	v_cvt_f32_i32_e32 v72, v72
	v_cvt_f32_i32_e32 v68, v68
	v_cvt_f32_i32_e32 v81, v81
	v_cvt_f32_i32_e32 v77, v77
	v_cvt_f32_i32_e32 v73, v73
	v_cvt_f32_i32_e32 v69, v69
	v_cvt_f32_i32_e32 v50, v50
	v_cvt_f32_i32_e32 v54, v54
	v_cvt_f32_i32_e32 v62, v62
	v_cvt_f32_i32_e32 v58, v58
	v_cvt_f32_i32_e32 v55, v55
	v_cvt_f32_i32_e32 v51, v51
	v_cvt_f32_i32_e32 v59, v59
	v_cvt_f32_i32_e32 v63, v63
	v_cvt_f32_i32_e32 v56, v56
	s_waitcnt vmcnt(0)
	v_mul_f32_e32 v155, v155, v189
	v_mul_f32_e32 v154, v154, v189
	v_mul_f32_e32 v158, v158, v189
	v_mul_f32_e32 v147, v147, v189
	v_fma_f32 v155, v95, v155, v103
	v_mul_f32_e32 v155, 0xbfb8aa3b, v155
	v_fma_f32 v154, v94, v154, v102
	v_exp_f32_e32 v155, v155
	v_mul_f32_e32 v154, 0xbfb8aa3b, v154
	v_fma_f32 v158, v106, v158, v110
	v_fma_f32 v147, v83, v147, v91
	v_exp_f32_e32 v154, v154
	v_mul_f32_e32 v146, v146, v189
	v_mul_f32_e32 v158, 0xbfb8aa3b, v158
	v_mul_f32_e32 v147, 0xbfb8aa3b, v147
	v_fma_f32 v146, v82, v146, v90
	v_exp_f32_e32 v158, v158
	v_exp_f32_e32 v147, v147
	v_add_f32_e32 v155, 1.0, v155
	v_mul_f32_e32 v150, v150, v189
	v_mul_f32_e32 v146, 0xbfb8aa3b, v146
	v_rcp_f32_e32 v155, v155
	v_fma_f32 v150, v86, v150, v98
	v_exp_f32_e32 v146, v146
	v_add_f32_e32 v154, 1.0, v154
	v_mul_f32_e32 v150, 0xbfb8aa3b, v150
	v_rcp_f32_e32 v154, v154
	v_exp_f32_e32 v150, v150
	v_add_f32_e32 v158, 1.0, v158
	v_add_f32_e32 v147, 1.0, v147
	v_mul_f32_e32 v160, v160, v189
	v_rcp_f32_e32 v158, v158
	v_rcp_f32_e32 v195, v147
	v_mul_f32_e32 v197, v147, v155
	v_mul_f32_e32 v147, v156, v189
	v_fma_f32 v160, v108, v160, v112
	v_add_f32_e32 v146, 1.0, v146
	v_fma_f32 v147, v96, v147, v104
	v_rcp_f32_e32 v193, v146
	v_mul_f32_e32 v196, v146, v154
	v_mul_f32_e32 v146, 0xbfb8aa3b, v160
	v_mul_f32_e32 v147, 0xbfb8aa3b, v147
	v_add_f32_e32 v150, 1.0, v150
	v_exp_f32_e32 v146, v146
	v_exp_f32_e32 v147, v147
	v_rcp_f32_e32 v192, v150
	v_mul_f32_e32 v158, v150, v158
	v_mul_f32_e32 v150, v152, v189
	v_mul_f32_e32 v148, v148, v189
	v_fma_f32 v150, v88, v150, v100
	v_fma_f32 v148, v84, v148, v92
	v_mul_f32_e32 v150, 0xbfb8aa3b, v150
	v_mul_f32_e32 v148, 0xbfb8aa3b, v148
	v_exp_f32_e32 v150, v150
	v_exp_f32_e32 v148, v148
	v_add_f32_e32 v146, 1.0, v146
	v_add_f32_e32 v147, 1.0, v147
	v_rcp_f32_e32 v146, v146
	v_rcp_f32_e32 v147, v147
	v_mul_f32_e32 v159, v159, v189
	v_add_f32_e32 v150, 1.0, v150
	v_add_f32_e32 v148, 1.0, v148
	v_fma_f32 v159, v107, v159, v111
	v_mul_f32_e32 v156, v150, v146
	v_mul_f32_e32 v160, v148, v147
	v_mul_f32_e32 v146, v161, v189
	v_mul_f32_e32 v147, v157, v189
	v_mul_f32_e32 v159, 0xbfb8aa3b, v159
	v_fma_f32 v146, v109, v146, v113
	v_fma_f32 v147, v97, v147, v105
	v_exp_f32_e32 v159, v159
	v_mul_f32_e32 v146, 0xbfb8aa3b, v146
	v_mul_f32_e32 v147, 0xbfb8aa3b, v147
	v_mul_f32_e32 v151, v151, v189
	v_rcp_f32_e32 v152, v148
	v_exp_f32_e32 v146, v146
	v_exp_f32_e32 v147, v147
	v_mul_f32_e32 v148, v153, v189
	v_mul_f32_e32 v149, v149, v189
	v_fma_f32 v151, v87, v151, v99
	v_fma_f32 v148, v89, v148, v101
	v_fma_f32 v149, v85, v149, v93
	v_mul_f32_e32 v151, 0xbfb8aa3b, v151
	v_mul_f32_e32 v148, 0xbfb8aa3b, v148
	v_mul_f32_e32 v149, 0xbfb8aa3b, v149
	v_exp_f32_e32 v151, v151
	v_add_f32_e32 v159, 1.0, v159
	v_exp_f32_e32 v148, v148
	v_exp_f32_e32 v149, v149
	v_rcp_f32_e32 v159, v159
	v_add_f32_e32 v146, 1.0, v146
	v_add_f32_e32 v147, 1.0, v147
	v_rcp_f32_e32 v146, v146
	v_rcp_f32_e32 v147, v147
	v_add_f32_e32 v151, 1.0, v151
	v_add_f32_e32 v148, 1.0, v148
	v_add_f32_e32 v149, 1.0, v149
	v_rcp_f32_e32 v194, v151
	v_mul_f32_e32 v159, v151, v159
	v_rcp_f32_e32 v151, v150
	v_rcp_f32_e32 v150, v148
	v_rcp_f32_e32 v153, v149
	v_mul_f32_e32 v157, v148, v146
	v_mul_f32_e32 v161, v149, v147
	v_cvt_pk_bf16_f32 v148, v192, v194
	v_cvt_pk_bf16_f32 v149, v151, v150
	v_cvt_pk_bf16_f32 v150, v193, v195
	v_cvt_pk_bf16_f32 v151, v152, v153
	v_lshlrev_b64 v[152:153], 12, v[182:183]
	v_lshl_add_u64 v[154:155], s[16:17], 0, v[152:153]
	v_lshlrev_b64 v[146:147], 1, v[190:191]
	v_lshl_add_u64 v[154:155], v[154:155], 0, v[146:147]
	v_lshl_add_u64 v[152:153], s[10:11], 0, v[152:153]
	global_store_dwordx4 v[154:155], v[148:151], off
	v_lshl_add_u64 v[152:153], v[152:153], 0, v[146:147]
	v_cvt_f32_i32_e32 v52, v52
	v_cvt_pk_bf16_f32 v148, v158, v159
	v_cvt_pk_bf16_f32 v149, v156, v157
	v_cvt_pk_bf16_f32 v150, v196, v197
	v_cvt_pk_bf16_f32 v151, v160, v161
	global_store_dwordx4 v[152:153], v[148:151], off
	v_cvt_f32_i32_e32 v60, v60
	v_cvt_f32_i32_e32 v64, v64
	v_add_u32_e32 v148, 16, v182
	v_ashrrev_i32_e32 v149, 31, v148
	v_lshl_add_u64 v[150:151], v[148:149], 2, s[12:13]
	v_mov_b32_e32 v150, v198
	v_cvt_f32_i32_e32 v57, v57
	v_cvt_f32_i32_e32 v53, v53
	v_cvt_f32_i32_e32 v61, v61
	v_cvt_f32_i32_e32 v65, v65
	v_cvt_f32_i32_e32 v34, v34
	v_cvt_f32_i32_e32 v38, v38
	v_cvt_f32_i32_e32 v46, v46
	v_cvt_f32_i32_e32 v42, v42
	v_cvt_f32_i32_e32 v39, v39
	v_cvt_f32_i32_e32 v35, v35
	v_cvt_f32_i32_e32 v43, v43
	v_cvt_f32_i32_e32 v47, v47
	v_cvt_f32_i32_e32 v40, v40
	v_cvt_f32_i32_e32 v36, v36
	v_cvt_f32_i32_e32 v44, v44
	v_cvt_f32_i32_e32 v48, v48
	v_cvt_f32_i32_e32 v41, v41
	v_cvt_f32_i32_e32 v37, v37
	v_cvt_f32_i32_e32 v45, v45
	v_cvt_f32_i32_e32 v49, v49
	v_cvt_f32_i32_e32 v18, v18
	v_cvt_f32_i32_e32 v22, v22
	v_cvt_f32_i32_e32 v30, v30
	v_cvt_f32_i32_e32 v26, v26
	v_cvt_f32_i32_e32 v23, v23
	v_cvt_f32_i32_e32 v19, v19
	v_cvt_f32_i32_e32 v27, v27
	v_cvt_f32_i32_e32 v31, v31
	v_cvt_f32_i32_e32 v24, v24
	v_cvt_f32_i32_e32 v20, v20
	v_cvt_f32_i32_e32 v28, v28
	v_cvt_f32_i32_e32 v32, v32
	v_cvt_f32_i32_e32 v25, v25
	v_cvt_f32_i32_e32 v21, v21
	v_cvt_f32_i32_e32 v29, v29
	v_cvt_f32_i32_e32 v33, v33
	v_cvt_f32_i32_e32 v2, v2
	v_cvt_f32_i32_e32 v6, v6
	v_cvt_f32_i32_e32 v14, v14
	v_cvt_f32_i32_e32 v10, v10
	v_cvt_f32_i32_e32 v7, v7
	v_cvt_f32_i32_e32 v3, v3
	v_cvt_f32_i32_e32 v11, v11
	v_cvt_f32_i32_e32 v15, v15
	v_cvt_f32_i32_e32 v8, v8
	v_cvt_f32_i32_e32 v4, v4
	v_cvt_f32_i32_e32 v12, v12
	v_cvt_f32_i32_e32 v16, v16
	v_cvt_f32_i32_e32 v9, v9
	v_cvt_f32_i32_e32 v5, v5
	v_cvt_f32_i32_e32 v13, v13
	v_cvt_f32_i32_e32 v17, v17
	s_andn2_b64 vcc, exec, s[6:7]
	s_mov_b64 s[6:7], -1
	v_mul_f32_e32 v142, v142, v150
	v_mul_f32_e32 v138, v138, v150
	v_fma_f32 v142, v106, v142, v110
	v_fma_f32 v138, v94, v138, v102
	v_mul_f32_e32 v142, 0xbfb8aa3b, v142
	v_mul_f32_e32 v138, 0xbfb8aa3b, v138
	v_exp_f32_e32 v142, v142
	v_exp_f32_e32 v138, v138
	v_mul_f32_e32 v134, v134, v150
	v_mul_f32_e32 v130, v130, v150
	v_fma_f32 v134, v86, v134, v98
	v_fma_f32 v130, v82, v130, v90
	v_mul_f32_e32 v134, 0xbfb8aa3b, v134
	v_mul_f32_e32 v130, 0xbfb8aa3b, v130
	v_exp_f32_e32 v134, v134
	v_exp_f32_e32 v130, v130
	v_add_f32_e32 v142, 1.0, v142
	v_add_f32_e32 v138, 1.0, v138
	v_rcp_f32_e32 v142, v142
	v_rcp_f32_e32 v138, v138
	v_add_f32_e32 v134, 1.0, v134
	v_add_f32_e32 v130, 1.0, v130
	v_rcp_f32_e32 v151, v134
	v_rcp_f32_e32 v152, v130
	v_mul_f32_e32 v142, v134, v142
	v_mul_f32_e32 v138, v130, v138
	v_mul_f32_e32 v130, v143, v150
	v_mul_f32_e32 v134, v139, v150
	v_fma_f32 v130, v107, v130, v111
	v_fma_f32 v134, v95, v134, v103
	v_mul_f32_e32 v130, 0xbfb8aa3b, v130
	v_mul_f32_e32 v134, 0xbfb8aa3b, v134
	v_exp_f32_e32 v130, v130
	v_exp_f32_e32 v134, v134
	v_mul_f32_e32 v135, v135, v150
	v_mul_f32_e32 v131, v131, v150
	v_fma_f32 v135, v87, v135, v99
	v_fma_f32 v131, v83, v131, v91
	v_mul_f32_e32 v135, 0xbfb8aa3b, v135
	v_mul_f32_e32 v131, 0xbfb8aa3b, v131
	v_exp_f32_e32 v135, v135
	v_exp_f32_e32 v131, v131
	v_add_f32_e32 v130, 1.0, v130
	v_add_f32_e32 v134, 1.0, v134
	v_rcp_f32_e32 v130, v130
	v_rcp_f32_e32 v134, v134
	v_add_f32_e32 v135, 1.0, v135
	v_add_f32_e32 v131, 1.0, v131
	v_rcp_f32_e32 v143, v131
	v_mul_f32_e32 v153, v135, v130
	v_mul_f32_e32 v154, v131, v134
	v_mul_f32_e32 v130, v144, v150
	v_mul_f32_e32 v131, v140, v150
	v_fma_f32 v130, v108, v130, v112
	v_fma_f32 v131, v96, v131, v104
	v_mul_f32_e32 v130, 0xbfb8aa3b, v130
	v_mul_f32_e32 v131, 0xbfb8aa3b, v131
	v_exp_f32_e32 v130, v130
	v_exp_f32_e32 v131, v131
	v_mul_f32_e32 v134, v136, v150
	v_mul_f32_e32 v132, v132, v150
	v_fma_f32 v134, v88, v134, v100
	v_fma_f32 v132, v84, v132, v92
	v_mul_f32_e32 v134, 0xbfb8aa3b, v134
	v_mul_f32_e32 v132, 0xbfb8aa3b, v132
	v_exp_f32_e32 v134, v134
	v_exp_f32_e32 v132, v132
	v_add_f32_e32 v130, 1.0, v130
	v_add_f32_e32 v131, 1.0, v131
	v_rcp_f32_e32 v130, v130
	v_rcp_f32_e32 v131, v131
	v_add_f32_e32 v134, 1.0, v134
	v_add_f32_e32 v132, 1.0, v132
	v_mul_f32_e32 v140, v134, v130
	v_mul_f32_e32 v144, v132, v131
	v_mul_f32_e32 v130, v145, v150
	v_mul_f32_e32 v131, v141, v150
	v_fma_f32 v130, v109, v130, v113
	v_fma_f32 v131, v97, v131, v105
	v_mul_f32_e32 v130, 0xbfb8aa3b, v130
	v_mul_f32_e32 v131, 0xbfb8aa3b, v131
	v_rcp_f32_e32 v136, v132
	v_exp_f32_e32 v130, v130
	v_exp_f32_e32 v131, v131
	v_mul_f32_e32 v132, v137, v150
	v_fma_f32 v132, v89, v132, v101
	v_mul_f32_e32 v133, v133, v150
	v_mul_f32_e32 v132, 0xbfb8aa3b, v132
	v_fma_f32 v133, v85, v133, v93
	v_exp_f32_e32 v132, v132
	v_mul_f32_e32 v133, 0xbfb8aa3b, v133
	v_exp_f32_e32 v133, v133
	v_add_f32_e32 v130, 1.0, v130
	v_add_f32_e32 v131, 1.0, v131
	v_rcp_f32_e32 v130, v130
	v_rcp_f32_e32 v131, v131
	v_add_f32_e32 v132, 1.0, v132
	v_rcp_f32_e32 v139, v135
	v_rcp_f32_e32 v135, v134
	v_add_f32_e32 v133, 1.0, v133
	v_rcp_f32_e32 v134, v132
	v_rcp_f32_e32 v137, v133
	v_mul_f32_e32 v141, v132, v130
	v_mul_f32_e32 v145, v133, v131
	v_cvt_pk_bf16_f32 v130, v151, v139
	v_cvt_pk_bf16_f32 v131, v135, v134
	v_lshlrev_b64 v[134:135], 12, v[148:149]
	v_cvt_pk_bf16_f32 v132, v152, v143
	v_cvt_pk_bf16_f32 v133, v136, v137
	v_lshl_add_u64 v[136:137], s[16:17], 0, v[134:135]
	v_lshl_add_u64 v[136:137], v[136:137], 0, v[146:147]
	v_lshl_add_u64 v[134:135], s[10:11], 0, v[134:135]
	global_store_dwordx4 v[136:137], v[130:133], off
	v_lshl_add_u64 v[134:135], v[134:135], 0, v[146:147]
	s_nop 0
	v_cvt_pk_bf16_f32 v130, v142, v153
	v_cvt_pk_bf16_f32 v131, v140, v141
	v_cvt_pk_bf16_f32 v132, v138, v154
	v_cvt_pk_bf16_f32 v133, v144, v145
	global_store_dwordx4 v[134:135], v[130:133], off
	s_nop 1
	v_add_u32_e32 v130, 32, v182
	v_ashrrev_i32_e32 v131, 31, v130
	v_lshl_add_u64 v[132:133], v[130:131], 2, s[12:13]
	v_mov_b32_e32 v132, v199
	v_mul_f32_e32 v126, v126, v132
	v_mul_f32_e32 v122, v122, v132
	v_fma_f32 v126, v106, v126, v110
	v_fma_f32 v122, v94, v122, v102
	v_mul_f32_e32 v126, 0xbfb8aa3b, v126
	v_mul_f32_e32 v122, 0xbfb8aa3b, v122
	v_exp_f32_e32 v126, v126
	v_exp_f32_e32 v122, v122
	v_mul_f32_e32 v118, v118, v132
	v_mul_f32_e32 v114, v114, v132
	v_fma_f32 v118, v86, v118, v98
	v_fma_f32 v114, v82, v114, v90
	v_mul_f32_e32 v118, 0xbfb8aa3b, v118
	v_mul_f32_e32 v114, 0xbfb8aa3b, v114
	v_exp_f32_e32 v118, v118
	v_exp_f32_e32 v114, v114
	v_add_f32_e32 v126, 1.0, v126
	v_add_f32_e32 v122, 1.0, v122
	v_rcp_f32_e32 v126, v126
	v_rcp_f32_e32 v122, v122
	v_add_f32_e32 v118, 1.0, v118
	v_add_f32_e32 v114, 1.0, v114
	v_rcp_f32_e32 v133, v118
	v_rcp_f32_e32 v134, v114
	v_mul_f32_e32 v126, v118, v126
	v_mul_f32_e32 v122, v114, v122
	v_mul_f32_e32 v114, v127, v132
	v_mul_f32_e32 v118, v123, v132
	v_fma_f32 v114, v107, v114, v111
	v_fma_f32 v118, v95, v118, v103
	v_mul_f32_e32 v114, 0xbfb8aa3b, v114
	v_mul_f32_e32 v118, 0xbfb8aa3b, v118
	v_exp_f32_e32 v114, v114
	v_exp_f32_e32 v118, v118
	v_mul_f32_e32 v119, v119, v132
	v_mul_f32_e32 v115, v115, v132
	v_fma_f32 v119, v87, v119, v99
	v_fma_f32 v115, v83, v115, v91
	v_mul_f32_e32 v119, 0xbfb8aa3b, v119
	v_mul_f32_e32 v115, 0xbfb8aa3b, v115
	v_exp_f32_e32 v119, v119
	v_exp_f32_e32 v115, v115
	v_add_f32_e32 v114, 1.0, v114
	v_add_f32_e32 v118, 1.0, v118
	v_rcp_f32_e32 v114, v114
	v_rcp_f32_e32 v118, v118
	v_add_f32_e32 v119, 1.0, v119
	v_add_f32_e32 v115, 1.0, v115
	v_rcp_f32_e32 v127, v115
	v_mul_f32_e32 v135, v119, v114
	v_mul_f32_e32 v136, v115, v118
	v_mul_f32_e32 v114, v128, v132
	v_mul_f32_e32 v115, v124, v132
	v_fma_f32 v114, v108, v114, v112
	v_fma_f32 v115, v96, v115, v104
	v_mul_f32_e32 v114, 0xbfb8aa3b, v114
	v_mul_f32_e32 v115, 0xbfb8aa3b, v115
	v_exp_f32_e32 v114, v114
	v_exp_f32_e32 v115, v115
	v_mul_f32_e32 v118, v120, v132
	v_mul_f32_e32 v116, v116, v132
	v_fma_f32 v118, v88, v118, v100
	v_fma_f32 v116, v84, v116, v92
	v_mul_f32_e32 v118, 0xbfb8aa3b, v118
	v_mul_f32_e32 v116, 0xbfb8aa3b, v116
	v_exp_f32_e32 v118, v118
	v_exp_f32_e32 v116, v116
	v_add_f32_e32 v114, 1.0, v114
	v_add_f32_e32 v115, 1.0, v115
	v_rcp_f32_e32 v114, v114
	v_rcp_f32_e32 v115, v115
	v_add_f32_e32 v118, 1.0, v118
	v_add_f32_e32 v116, 1.0, v116
	v_mul_f32_e32 v124, v118, v114
	v_mul_f32_e32 v128, v116, v115
	v_mul_f32_e32 v114, v129, v132
	v_mul_f32_e32 v115, v125, v132
	v_fma_f32 v114, v109, v114, v113
	v_fma_f32 v115, v97, v115, v105
	v_mul_f32_e32 v114, 0xbfb8aa3b, v114
	v_mul_f32_e32 v115, 0xbfb8aa3b, v115
	v_rcp_f32_e32 v120, v116
	v_exp_f32_e32 v114, v114
	v_exp_f32_e32 v115, v115
	v_mul_f32_e32 v116, v121, v132
	v_fma_f32 v116, v89, v116, v101
	v_mul_f32_e32 v117, v117, v132
	v_mul_f32_e32 v116, 0xbfb8aa3b, v116
	v_fma_f32 v117, v85, v117, v93
	v_exp_f32_e32 v116, v116
	v_mul_f32_e32 v117, 0xbfb8aa3b, v117
	v_exp_f32_e32 v117, v117
	v_add_f32_e32 v114, 1.0, v114
	v_add_f32_e32 v115, 1.0, v115
	v_rcp_f32_e32 v114, v114
	v_rcp_f32_e32 v115, v115
	v_add_f32_e32 v116, 1.0, v116
	v_rcp_f32_e32 v123, v119
	v_rcp_f32_e32 v119, v118
	v_add_f32_e32 v117, 1.0, v117
	v_rcp_f32_e32 v118, v116
	v_rcp_f32_e32 v121, v117
	v_mul_f32_e32 v125, v116, v114
	v_mul_f32_e32 v129, v117, v115
	v_cvt_pk_bf16_f32 v114, v133, v123
	v_cvt_pk_bf16_f32 v115, v119, v118
	v_lshlrev_b64 v[118:119], 12, v[130:131]
	v_cvt_pk_bf16_f32 v116, v134, v127
	v_cvt_pk_bf16_f32 v117, v120, v121
	v_lshl_add_u64 v[120:121], s[16:17], 0, v[118:119]
	v_lshl_add_u64 v[120:121], v[120:121], 0, v[146:147]
	v_lshl_add_u64 v[118:119], s[10:11], 0, v[118:119]
	global_store_dwordx4 v[120:121], v[114:117], off
	v_lshl_add_u64 v[118:119], v[118:119], 0, v[146:147]
	s_nop 0
	v_cvt_pk_bf16_f32 v114, v126, v135
	v_cvt_pk_bf16_f32 v115, v124, v125
	v_cvt_pk_bf16_f32 v116, v122, v136
	v_cvt_pk_bf16_f32 v117, v128, v129
	global_store_dwordx4 v[118:119], v[114:117], off
	s_nop 1
	v_add_u32_e32 v114, 48, v182
	v_ashrrev_i32_e32 v115, 31, v114
	v_lshl_add_u64 v[116:117], v[114:115], 2, s[12:13]
	v_mov_b32_e32 v116, v200
	v_mul_f32_e32 v78, v78, v116
	v_mul_f32_e32 v74, v74, v116
	v_fma_f32 v78, v106, v78, v110
	v_fma_f32 v74, v94, v74, v102
	v_mul_f32_e32 v78, 0xbfb8aa3b, v78
	v_mul_f32_e32 v74, 0xbfb8aa3b, v74
	v_exp_f32_e32 v78, v78
	v_exp_f32_e32 v74, v74
	v_mul_f32_e32 v70, v70, v116
	v_mul_f32_e32 v66, v66, v116
	v_fma_f32 v70, v86, v70, v98
	v_fma_f32 v66, v82, v66, v90
	v_mul_f32_e32 v70, 0xbfb8aa3b, v70
	v_mul_f32_e32 v66, 0xbfb8aa3b, v66
	v_exp_f32_e32 v70, v70
	v_exp_f32_e32 v66, v66
	v_add_f32_e32 v78, 1.0, v78
	v_add_f32_e32 v74, 1.0, v74
	v_rcp_f32_e32 v78, v78
	v_rcp_f32_e32 v74, v74
	v_add_f32_e32 v70, 1.0, v70
	v_add_f32_e32 v66, 1.0, v66
	v_rcp_f32_e32 v117, v70
	v_rcp_f32_e32 v118, v66
	v_mul_f32_e32 v78, v70, v78
	v_mul_f32_e32 v74, v66, v74
	v_mul_f32_e32 v66, v79, v116
	v_mul_f32_e32 v70, v75, v116
	v_fma_f32 v66, v107, v66, v111
	v_fma_f32 v70, v95, v70, v103
	v_mul_f32_e32 v66, 0xbfb8aa3b, v66
	v_mul_f32_e32 v70, 0xbfb8aa3b, v70
	v_exp_f32_e32 v66, v66
	v_exp_f32_e32 v70, v70
	v_mul_f32_e32 v71, v71, v116
	v_mul_f32_e32 v67, v67, v116
	v_fma_f32 v71, v87, v71, v99
	v_fma_f32 v67, v83, v67, v91
	v_mul_f32_e32 v71, 0xbfb8aa3b, v71
	v_mul_f32_e32 v67, 0xbfb8aa3b, v67
	v_exp_f32_e32 v71, v71
	v_exp_f32_e32 v67, v67
	v_add_f32_e32 v66, 1.0, v66
	v_add_f32_e32 v70, 1.0, v70
	v_rcp_f32_e32 v66, v66
	v_rcp_f32_e32 v70, v70
	v_add_f32_e32 v71, 1.0, v71
	v_add_f32_e32 v67, 1.0, v67
	v_rcp_f32_e32 v79, v67
	v_mul_f32_e32 v119, v71, v66
	v_mul_f32_e32 v120, v67, v70
	v_mul_f32_e32 v66, v80, v116
	v_mul_f32_e32 v67, v76, v116
	v_fma_f32 v66, v108, v66, v112
	v_fma_f32 v67, v96, v67, v104
	v_mul_f32_e32 v66, 0xbfb8aa3b, v66
	v_mul_f32_e32 v67, 0xbfb8aa3b, v67
	v_exp_f32_e32 v66, v66
	v_exp_f32_e32 v67, v67
	v_mul_f32_e32 v70, v72, v116
	v_mul_f32_e32 v68, v68, v116
	v_fma_f32 v70, v88, v70, v100
	v_fma_f32 v68, v84, v68, v92
	v_mul_f32_e32 v70, 0xbfb8aa3b, v70
	v_mul_f32_e32 v68, 0xbfb8aa3b, v68
	v_exp_f32_e32 v70, v70
	v_exp_f32_e32 v68, v68
	v_add_f32_e32 v66, 1.0, v66
	v_add_f32_e32 v67, 1.0, v67
	v_rcp_f32_e32 v66, v66
	v_rcp_f32_e32 v67, v67
	v_add_f32_e32 v70, 1.0, v70
	v_add_f32_e32 v68, 1.0, v68
	v_mul_f32_e32 v76, v70, v66
	v_mul_f32_e32 v80, v68, v67
	v_mul_f32_e32 v66, v81, v116
	v_mul_f32_e32 v67, v77, v116
	v_fma_f32 v66, v109, v66, v113
	v_fma_f32 v67, v97, v67, v105
	v_mul_f32_e32 v66, 0xbfb8aa3b, v66
	v_mul_f32_e32 v67, 0xbfb8aa3b, v67
	v_rcp_f32_e32 v72, v68
	v_exp_f32_e32 v66, v66
	v_exp_f32_e32 v67, v67
	v_mul_f32_e32 v68, v73, v116
	v_fma_f32 v68, v89, v68, v101
	v_mul_f32_e32 v69, v69, v116
	v_mul_f32_e32 v68, 0xbfb8aa3b, v68
	v_fma_f32 v69, v85, v69, v93
	v_exp_f32_e32 v68, v68
	v_mul_f32_e32 v69, 0xbfb8aa3b, v69
	v_exp_f32_e32 v69, v69
	v_add_f32_e32 v66, 1.0, v66
	v_add_f32_e32 v67, 1.0, v67
	v_rcp_f32_e32 v66, v66
	v_rcp_f32_e32 v67, v67
	v_add_f32_e32 v68, 1.0, v68
	v_rcp_f32_e32 v75, v71
	v_rcp_f32_e32 v71, v70
	v_add_f32_e32 v69, 1.0, v69
	v_rcp_f32_e32 v70, v68
	v_rcp_f32_e32 v73, v69
	v_mul_f32_e32 v77, v68, v66
	v_mul_f32_e32 v81, v69, v67
	v_cvt_pk_bf16_f32 v66, v117, v75
	v_cvt_pk_bf16_f32 v67, v71, v70
	v_lshlrev_b64 v[70:71], 12, v[114:115]
	v_cvt_pk_bf16_f32 v68, v118, v79
	v_cvt_pk_bf16_f32 v69, v72, v73
	v_lshl_add_u64 v[72:73], s[16:17], 0, v[70:71]
	v_lshl_add_u64 v[72:73], v[72:73], 0, v[146:147]
	v_lshl_add_u64 v[70:71], s[10:11], 0, v[70:71]
	global_store_dwordx4 v[72:73], v[66:69], off
	v_lshl_add_u64 v[70:71], v[70:71], 0, v[146:147]
	s_nop 0
	v_cvt_pk_bf16_f32 v66, v78, v119
	v_cvt_pk_bf16_f32 v67, v76, v77
	v_cvt_pk_bf16_f32 v68, v74, v120
	v_cvt_pk_bf16_f32 v69, v80, v81
	global_store_dwordx4 v[70:71], v[66:69], off
	s_nop 1
	v_add_u32_e32 v66, 0x80, v182
	v_ashrrev_i32_e32 v67, 31, v66
	v_lshl_add_u64 v[68:69], v[66:67], 2, s[12:13]
	v_mov_b32_e32 v68, v201
	v_mul_f32_e32 v50, v50, v68
	v_fma_f32 v50, v94, v50, v102
	v_mul_f32_e32 v50, 0xbfb8aa3b, v50
	v_exp_f32_e32 v50, v50
	v_mul_f32_e32 v54, v54, v68
	v_mul_f32_e32 v62, v62, v68
	v_fma_f32 v54, v106, v54, v110
	v_fma_f32 v62, v82, v62, v90
	v_mul_f32_e32 v54, 0xbfb8aa3b, v54
	v_mul_f32_e32 v62, 0xbfb8aa3b, v62
	v_exp_f32_e32 v54, v54
	v_exp_f32_e32 v62, v62
	v_add_f32_e32 v50, 1.0, v50
	v_mul_f32_e32 v58, v58, v68
	v_rcp_f32_e32 v50, v50
	v_fma_f32 v58, v86, v58, v98
	v_mul_f32_e32 v58, 0xbfb8aa3b, v58
	v_exp_f32_e32 v58, v58
	v_add_f32_e32 v54, 1.0, v54
	v_add_f32_e32 v62, 1.0, v62
	v_rcp_f32_e32 v54, v54
	v_rcp_f32_e32 v70, v62
	v_mul_f32_e32 v62, v62, v50
	v_mul_f32_e32 v50, v55, v68
	v_mul_f32_e32 v51, v51, v68
	v_fma_f32 v50, v107, v50, v111
	v_fma_f32 v51, v95, v51, v103
	v_mul_f32_e32 v50, 0xbfb8aa3b, v50
	v_mul_f32_e32 v51, 0xbfb8aa3b, v51
	v_add_f32_e32 v58, 1.0, v58
	v_exp_f32_e32 v50, v50
	v_exp_f32_e32 v51, v51
	v_rcp_f32_e32 v69, v58
	v_mul_f32_e32 v58, v58, v54
	v_mul_f32_e32 v54, v59, v68
	v_mul_f32_e32 v55, v63, v68
	v_fma_f32 v54, v87, v54, v99
	v_fma_f32 v55, v83, v55, v91
	v_mul_f32_e32 v54, 0xbfb8aa3b, v54
	v_mul_f32_e32 v55, 0xbfb8aa3b, v55
	v_exp_f32_e32 v54, v54
	v_exp_f32_e32 v55, v55
	v_add_f32_e32 v50, 1.0, v50
	v_add_f32_e32 v51, 1.0, v51
	v_rcp_f32_e32 v50, v50
	v_rcp_f32_e32 v51, v51
	v_add_f32_e32 v54, 1.0, v54
	v_add_f32_e32 v55, 1.0, v55
	v_mul_f32_e32 v71, v54, v50
	v_mul_f32_e32 v72, v55, v51
	v_mul_f32_e32 v50, v56, v68
	v_mul_f32_e32 v51, v52, v68
	v_fma_f32 v50, v108, v50, v112
	v_fma_f32 v51, v96, v51, v104
	v_mul_f32_e32 v50, 0xbfb8aa3b, v50
	v_mul_f32_e32 v51, 0xbfb8aa3b, v51
	v_exp_f32_e32 v50, v50
	v_exp_f32_e32 v51, v51
	v_rcp_f32_e32 v59, v54
	v_mul_f32_e32 v52, v60, v68
	v_mul_f32_e32 v54, v64, v68
	v_fma_f32 v52, v88, v52, v100
	v_fma_f32 v54, v84, v54, v92
	v_mul_f32_e32 v52, 0xbfb8aa3b, v52
	v_mul_f32_e32 v54, 0xbfb8aa3b, v54
	v_exp_f32_e32 v52, v52
	v_exp_f32_e32 v54, v54
	v_add_f32_e32 v50, 1.0, v50
	v_add_f32_e32 v51, 1.0, v51
	v_rcp_f32_e32 v50, v50
	v_rcp_f32_e32 v51, v51
	v_add_f32_e32 v52, 1.0, v52
	v_add_f32_e32 v54, 1.0, v54
	v_mul_f32_e32 v60, v52, v50
	v_mul_f32_e32 v64, v54, v51
	v_mul_f32_e32 v50, v57, v68
	v_mul_f32_e32 v51, v53, v68
	v_fma_f32 v50, v109, v50, v113
	v_fma_f32 v51, v97, v51, v105
	v_mul_f32_e32 v50, 0xbfb8aa3b, v50
	v_mul_f32_e32 v51, 0xbfb8aa3b, v51
	v_rcp_f32_e32 v63, v55
	v_rcp_f32_e32 v55, v52
	v_exp_f32_e32 v50, v50
	v_exp_f32_e32 v51, v51
	v_mul_f32_e32 v52, v61, v68
	v_fma_f32 v52, v89, v52, v101
	v_mul_f32_e32 v53, v65, v68
	v_mul_f32_e32 v52, 0xbfb8aa3b, v52
	v_fma_f32 v53, v85, v53, v93
	v_exp_f32_e32 v52, v52
	v_mul_f32_e32 v53, 0xbfb8aa3b, v53
	v_exp_f32_e32 v53, v53
	v_add_f32_e32 v50, 1.0, v50
	v_add_f32_e32 v51, 1.0, v51
	v_rcp_f32_e32 v50, v50
	v_rcp_f32_e32 v51, v51
	v_add_f32_e32 v52, 1.0, v52
	v_rcp_f32_e32 v56, v54
	v_add_f32_e32 v53, 1.0, v53
	v_rcp_f32_e32 v54, v52
	v_rcp_f32_e32 v57, v53
	v_mul_f32_e32 v61, v52, v50
	v_mul_f32_e32 v65, v53, v51
	v_cvt_pk_bf16_f32 v50, v69, v59
	v_cvt_pk_bf16_f32 v51, v55, v54
	v_lshlrev_b64 v[54:55], 12, v[66:67]
	v_cvt_pk_bf16_f32 v52, v70, v63
	v_cvt_pk_bf16_f32 v53, v56, v57
	v_lshl_add_u64 v[56:57], s[16:17], 0, v[54:55]
	v_lshl_add_u64 v[56:57], v[56:57], 0, v[146:147]
	v_lshl_add_u64 v[54:55], s[10:11], 0, v[54:55]
	global_store_dwordx4 v[56:57], v[50:53], off
	v_lshl_add_u64 v[54:55], v[54:55], 0, v[146:147]
	s_nop 0
	v_cvt_pk_bf16_f32 v50, v58, v71
	v_cvt_pk_bf16_f32 v51, v60, v61
	v_cvt_pk_bf16_f32 v52, v62, v72
	v_cvt_pk_bf16_f32 v53, v64, v65
	global_store_dwordx4 v[54:55], v[50:53], off
	s_nop 1
	v_add_u32_e32 v50, 0x90, v182
	v_ashrrev_i32_e32 v51, 31, v50
	v_lshl_add_u64 v[52:53], v[50:51], 2, s[12:13]
	v_mov_b32_e32 v52, v202
	v_mul_f32_e32 v34, v34, v52
	v_fma_f32 v34, v94, v34, v102
	v_mul_f32_e32 v34, 0xbfb8aa3b, v34
	v_exp_f32_e32 v34, v34
	v_mul_f32_e32 v38, v38, v52
	v_mul_f32_e32 v46, v46, v52
	v_fma_f32 v38, v106, v38, v110
	v_fma_f32 v46, v82, v46, v90
	v_mul_f32_e32 v38, 0xbfb8aa3b, v38
	v_mul_f32_e32 v46, 0xbfb8aa3b, v46
	v_exp_f32_e32 v38, v38
	v_exp_f32_e32 v46, v46
	v_add_f32_e32 v34, 1.0, v34
	v_mul_f32_e32 v42, v42, v52
	v_rcp_f32_e32 v34, v34
	v_fma_f32 v42, v86, v42, v98
	v_mul_f32_e32 v42, 0xbfb8aa3b, v42
	v_exp_f32_e32 v42, v42
	v_add_f32_e32 v38, 1.0, v38
	v_add_f32_e32 v46, 1.0, v46
	v_rcp_f32_e32 v38, v38
	v_rcp_f32_e32 v54, v46
	v_mul_f32_e32 v46, v46, v34
	v_mul_f32_e32 v34, v39, v52
	v_mul_f32_e32 v35, v35, v52
	v_fma_f32 v34, v107, v34, v111
	v_fma_f32 v35, v95, v35, v103
	v_mul_f32_e32 v34, 0xbfb8aa3b, v34
	v_mul_f32_e32 v35, 0xbfb8aa3b, v35
	v_add_f32_e32 v42, 1.0, v42
	v_exp_f32_e32 v34, v34
	v_exp_f32_e32 v35, v35
	v_rcp_f32_e32 v53, v42
	v_mul_f32_e32 v42, v42, v38
	v_mul_f32_e32 v38, v43, v52
	v_mul_f32_e32 v39, v47, v52
	v_fma_f32 v38, v87, v38, v99
	v_fma_f32 v39, v83, v39, v91
	v_mul_f32_e32 v38, 0xbfb8aa3b, v38
	v_mul_f32_e32 v39, 0xbfb8aa3b, v39
	v_exp_f32_e32 v38, v38
	v_exp_f32_e32 v39, v39
	v_add_f32_e32 v34, 1.0, v34
	v_add_f32_e32 v35, 1.0, v35
	v_rcp_f32_e32 v34, v34
	v_rcp_f32_e32 v35, v35
	v_add_f32_e32 v38, 1.0, v38
	v_add_f32_e32 v39, 1.0, v39
	v_mul_f32_e32 v55, v38, v34
	v_mul_f32_e32 v56, v39, v35
	v_mul_f32_e32 v34, v40, v52
	v_mul_f32_e32 v35, v36, v52
	v_fma_f32 v34, v108, v34, v112
	v_fma_f32 v35, v96, v35, v104
	v_mul_f32_e32 v34, 0xbfb8aa3b, v34
	v_mul_f32_e32 v35, 0xbfb8aa3b, v35
	v_exp_f32_e32 v34, v34
	v_exp_f32_e32 v35, v35
	v_rcp_f32_e32 v43, v38
	v_mul_f32_e32 v36, v44, v52
	v_mul_f32_e32 v38, v48, v52
	v_fma_f32 v36, v88, v36, v100
	v_fma_f32 v38, v84, v38, v92
	v_mul_f32_e32 v36, 0xbfb8aa3b, v36
	v_mul_f32_e32 v38, 0xbfb8aa3b, v38
	v_exp_f32_e32 v36, v36
	v_exp_f32_e32 v38, v38
	v_add_f32_e32 v34, 1.0, v34
	v_add_f32_e32 v35, 1.0, v35
	v_rcp_f32_e32 v34, v34
	v_rcp_f32_e32 v35, v35
	v_add_f32_e32 v36, 1.0, v36
	v_add_f32_e32 v38, 1.0, v38
	v_mul_f32_e32 v44, v36, v34
	v_mul_f32_e32 v48, v38, v35
	v_mul_f32_e32 v34, v41, v52
	v_mul_f32_e32 v35, v37, v52
	v_fma_f32 v34, v109, v34, v113
	v_fma_f32 v35, v97, v35, v105
	v_mul_f32_e32 v34, 0xbfb8aa3b, v34
	v_mul_f32_e32 v35, 0xbfb8aa3b, v35
	v_rcp_f32_e32 v47, v39
	v_rcp_f32_e32 v39, v36
	v_exp_f32_e32 v34, v34
	v_exp_f32_e32 v35, v35
	v_mul_f32_e32 v36, v45, v52
	v_fma_f32 v36, v89, v36, v101
	v_mul_f32_e32 v37, v49, v52
	v_mul_f32_e32 v36, 0xbfb8aa3b, v36
	v_fma_f32 v37, v85, v37, v93
	v_exp_f32_e32 v36, v36
	v_mul_f32_e32 v37, 0xbfb8aa3b, v37
	v_exp_f32_e32 v37, v37
	v_add_f32_e32 v34, 1.0, v34
	v_add_f32_e32 v35, 1.0, v35
	v_rcp_f32_e32 v34, v34
	v_rcp_f32_e32 v35, v35
	v_add_f32_e32 v36, 1.0, v36
	v_rcp_f32_e32 v40, v38
	v_add_f32_e32 v37, 1.0, v37
	v_rcp_f32_e32 v38, v36
	v_rcp_f32_e32 v41, v37
	v_mul_f32_e32 v45, v36, v34
	v_mul_f32_e32 v49, v37, v35
	v_cvt_pk_bf16_f32 v34, v53, v43
	v_cvt_pk_bf16_f32 v35, v39, v38
	v_lshlrev_b64 v[38:39], 12, v[50:51]
	v_cvt_pk_bf16_f32 v36, v54, v47
	v_cvt_pk_bf16_f32 v37, v40, v41
	v_lshl_add_u64 v[40:41], s[16:17], 0, v[38:39]
	v_lshl_add_u64 v[40:41], v[40:41], 0, v[146:147]
	v_lshl_add_u64 v[38:39], s[10:11], 0, v[38:39]
	global_store_dwordx4 v[40:41], v[34:37], off
	v_lshl_add_u64 v[38:39], v[38:39], 0, v[146:147]
	s_nop 0
	v_cvt_pk_bf16_f32 v34, v42, v55
	v_cvt_pk_bf16_f32 v35, v44, v45
	v_cvt_pk_bf16_f32 v36, v46, v56
	v_cvt_pk_bf16_f32 v37, v48, v49
	global_store_dwordx4 v[38:39], v[34:37], off
	s_nop 1
	v_add_u32_e32 v34, 0xa0, v182
	v_ashrrev_i32_e32 v35, 31, v34
	v_lshl_add_u64 v[36:37], v[34:35], 2, s[12:13]
	v_mov_b32_e32 v36, v203
	v_mul_f32_e32 v18, v18, v36
	v_fma_f32 v18, v94, v18, v102
	v_mul_f32_e32 v18, 0xbfb8aa3b, v18
	v_exp_f32_e32 v18, v18
	v_mul_f32_e32 v22, v22, v36
	v_mul_f32_e32 v30, v30, v36
	v_fma_f32 v22, v106, v22, v110
	v_fma_f32 v30, v82, v30, v90
	v_mul_f32_e32 v22, 0xbfb8aa3b, v22
	v_mul_f32_e32 v30, 0xbfb8aa3b, v30
	v_exp_f32_e32 v22, v22
	v_exp_f32_e32 v30, v30
	v_add_f32_e32 v18, 1.0, v18
	v_mul_f32_e32 v26, v26, v36
	v_rcp_f32_e32 v18, v18
	v_fma_f32 v26, v86, v26, v98
	v_mul_f32_e32 v26, 0xbfb8aa3b, v26
	v_exp_f32_e32 v26, v26
	v_add_f32_e32 v22, 1.0, v22
	v_add_f32_e32 v30, 1.0, v30
	v_rcp_f32_e32 v22, v22
	v_rcp_f32_e32 v38, v30
	v_mul_f32_e32 v30, v30, v18
	v_mul_f32_e32 v18, v23, v36
	v_mul_f32_e32 v19, v19, v36
	v_fma_f32 v18, v107, v18, v111
	v_fma_f32 v19, v95, v19, v103
	v_mul_f32_e32 v18, 0xbfb8aa3b, v18
	v_mul_f32_e32 v19, 0xbfb8aa3b, v19
	v_add_f32_e32 v26, 1.0, v26
	v_exp_f32_e32 v18, v18
	v_exp_f32_e32 v19, v19
	v_rcp_f32_e32 v37, v26
	v_mul_f32_e32 v26, v26, v22
	v_mul_f32_e32 v22, v27, v36
	v_mul_f32_e32 v23, v31, v36
	v_fma_f32 v22, v87, v22, v99
	v_fma_f32 v23, v83, v23, v91
	v_mul_f32_e32 v22, 0xbfb8aa3b, v22
	v_mul_f32_e32 v23, 0xbfb8aa3b, v23
	v_exp_f32_e32 v22, v22
	v_exp_f32_e32 v23, v23
	v_add_f32_e32 v18, 1.0, v18
	v_add_f32_e32 v19, 1.0, v19
	v_rcp_f32_e32 v18, v18
	v_rcp_f32_e32 v19, v19
	v_add_f32_e32 v22, 1.0, v22
	v_add_f32_e32 v23, 1.0, v23
	v_mul_f32_e32 v39, v22, v18
	v_mul_f32_e32 v40, v23, v19
	v_mul_f32_e32 v18, v24, v36
	v_mul_f32_e32 v19, v20, v36
	v_fma_f32 v18, v108, v18, v112
	v_fma_f32 v19, v96, v19, v104
	v_mul_f32_e32 v18, 0xbfb8aa3b, v18
	v_mul_f32_e32 v19, 0xbfb8aa3b, v19
	v_exp_f32_e32 v18, v18
	v_exp_f32_e32 v19, v19
	v_rcp_f32_e32 v27, v22
	v_mul_f32_e32 v20, v28, v36
	v_mul_f32_e32 v22, v32, v36
	v_fma_f32 v20, v88, v20, v100
	v_fma_f32 v22, v84, v22, v92
	v_mul_f32_e32 v20, 0xbfb8aa3b, v20
	v_mul_f32_e32 v22, 0xbfb8aa3b, v22
	v_exp_f32_e32 v20, v20
	v_exp_f32_e32 v22, v22
	v_add_f32_e32 v18, 1.0, v18
	v_add_f32_e32 v19, 1.0, v19
	v_rcp_f32_e32 v18, v18
	v_rcp_f32_e32 v19, v19
	v_add_f32_e32 v20, 1.0, v20
	v_add_f32_e32 v22, 1.0, v22
	v_mul_f32_e32 v28, v20, v18
	v_mul_f32_e32 v32, v22, v19
	v_mul_f32_e32 v18, v25, v36
	v_mul_f32_e32 v19, v21, v36
	v_fma_f32 v18, v109, v18, v113
	v_fma_f32 v19, v97, v19, v105
	v_mul_f32_e32 v18, 0xbfb8aa3b, v18
	v_mul_f32_e32 v19, 0xbfb8aa3b, v19
	v_rcp_f32_e32 v31, v23
	v_rcp_f32_e32 v23, v20
	v_exp_f32_e32 v18, v18
	v_exp_f32_e32 v19, v19
	v_mul_f32_e32 v20, v29, v36
	v_fma_f32 v20, v89, v20, v101
	v_mul_f32_e32 v21, v33, v36
	v_mul_f32_e32 v20, 0xbfb8aa3b, v20
	v_fma_f32 v21, v85, v21, v93
	v_exp_f32_e32 v20, v20
	v_mul_f32_e32 v21, 0xbfb8aa3b, v21
	v_exp_f32_e32 v21, v21
	v_add_f32_e32 v18, 1.0, v18
	v_add_f32_e32 v19, 1.0, v19
	v_rcp_f32_e32 v18, v18
	v_rcp_f32_e32 v19, v19
	v_add_f32_e32 v20, 1.0, v20
	v_rcp_f32_e32 v24, v22
	v_add_f32_e32 v21, 1.0, v21
	v_rcp_f32_e32 v22, v20
	v_rcp_f32_e32 v25, v21
	v_mul_f32_e32 v29, v20, v18
	v_mul_f32_e32 v33, v21, v19
	v_cvt_pk_bf16_f32 v18, v37, v27
	v_cvt_pk_bf16_f32 v19, v23, v22
	v_lshlrev_b64 v[22:23], 12, v[34:35]
	v_cvt_pk_bf16_f32 v20, v38, v31
	v_cvt_pk_bf16_f32 v21, v24, v25
	v_lshl_add_u64 v[24:25], s[16:17], 0, v[22:23]
	v_lshl_add_u64 v[24:25], v[24:25], 0, v[146:147]
	v_lshl_add_u64 v[22:23], s[10:11], 0, v[22:23]
	global_store_dwordx4 v[24:25], v[18:21], off
	v_lshl_add_u64 v[22:23], v[22:23], 0, v[146:147]
	s_nop 0
	v_cvt_pk_bf16_f32 v18, v26, v39
	v_cvt_pk_bf16_f32 v19, v28, v29
	v_cvt_pk_bf16_f32 v20, v30, v40
	v_cvt_pk_bf16_f32 v21, v32, v33
	global_store_dwordx4 v[22:23], v[18:21], off
	s_nop 1
	v_add_u32_e32 v18, 0xb0, v182
	v_ashrrev_i32_e32 v19, 31, v18
	v_lshl_add_u64 v[20:21], v[18:19], 2, s[12:13]
	v_mov_b32_e32 v20, v204
	v_mul_f32_e32 v2, v2, v20
	v_fma_f32 v2, v94, v2, v102
	v_mul_f32_e32 v2, 0xbfb8aa3b, v2
	v_exp_f32_e32 v2, v2
	v_mul_f32_e32 v6, v6, v20
	v_mul_f32_e32 v14, v14, v20
	v_fma_f32 v6, v106, v6, v110
	v_fma_f32 v14, v82, v14, v90
	v_mul_f32_e32 v6, 0xbfb8aa3b, v6
	v_mul_f32_e32 v14, 0xbfb8aa3b, v14
	v_exp_f32_e32 v6, v6
	v_exp_f32_e32 v14, v14
	v_add_f32_e32 v2, 1.0, v2
	v_mul_f32_e32 v10, v10, v20
	v_rcp_f32_e32 v2, v2
	v_fma_f32 v10, v86, v10, v98
	v_mul_f32_e32 v10, 0xbfb8aa3b, v10
	v_exp_f32_e32 v10, v10
	v_add_f32_e32 v6, 1.0, v6
	v_add_f32_e32 v14, 1.0, v14
	v_rcp_f32_e32 v6, v6
	v_rcp_f32_e32 v22, v14
	v_mul_f32_e32 v14, v14, v2
	v_mul_f32_e32 v2, v7, v20
	v_mul_f32_e32 v3, v3, v20
	v_fma_f32 v2, v107, v2, v111
	v_fma_f32 v3, v95, v3, v103
	v_mul_f32_e32 v2, 0xbfb8aa3b, v2
	v_mul_f32_e32 v3, 0xbfb8aa3b, v3
	v_add_f32_e32 v10, 1.0, v10
	v_exp_f32_e32 v2, v2
	v_exp_f32_e32 v3, v3
	v_rcp_f32_e32 v21, v10
	v_mul_f32_e32 v10, v10, v6
	v_mul_f32_e32 v6, v11, v20
	v_mul_f32_e32 v7, v15, v20
	v_fma_f32 v6, v87, v6, v99
	v_fma_f32 v7, v83, v7, v91
	v_mul_f32_e32 v6, 0xbfb8aa3b, v6
	v_mul_f32_e32 v7, 0xbfb8aa3b, v7
	v_exp_f32_e32 v6, v6
	v_exp_f32_e32 v7, v7
	v_add_f32_e32 v2, 1.0, v2
	v_add_f32_e32 v3, 1.0, v3
	v_rcp_f32_e32 v2, v2
	v_rcp_f32_e32 v3, v3
	v_add_f32_e32 v6, 1.0, v6
	v_add_f32_e32 v7, 1.0, v7
	v_mul_f32_e32 v23, v6, v2
	v_mul_f32_e32 v24, v7, v3
	v_mul_f32_e32 v2, v8, v20
	v_mul_f32_e32 v3, v4, v20
	v_fma_f32 v2, v108, v2, v112
	v_fma_f32 v3, v96, v3, v104
	v_mul_f32_e32 v2, 0xbfb8aa3b, v2
	v_mul_f32_e32 v3, 0xbfb8aa3b, v3
	v_exp_f32_e32 v2, v2
	v_exp_f32_e32 v3, v3
	v_rcp_f32_e32 v11, v6
	v_mul_f32_e32 v4, v12, v20
	v_mul_f32_e32 v6, v16, v20
	v_fma_f32 v4, v88, v4, v100
	v_fma_f32 v6, v84, v6, v92
	v_mul_f32_e32 v4, 0xbfb8aa3b, v4
	v_mul_f32_e32 v6, 0xbfb8aa3b, v6
	v_exp_f32_e32 v4, v4
	v_exp_f32_e32 v6, v6
	v_add_f32_e32 v2, 1.0, v2
	v_add_f32_e32 v3, 1.0, v3
	v_rcp_f32_e32 v2, v2
	v_rcp_f32_e32 v3, v3
	v_add_f32_e32 v4, 1.0, v4
	v_add_f32_e32 v6, 1.0, v6
	v_mul_f32_e32 v12, v4, v2
	v_mul_f32_e32 v16, v6, v3
	v_mul_f32_e32 v2, v9, v20
	v_mul_f32_e32 v3, v5, v20
	v_fmac_f32_e32 v113, v109, v2
	v_fmac_f32_e32 v105, v97, v3
	v_mul_f32_e32 v2, 0xbfb8aa3b, v113
	v_mul_f32_e32 v3, 0xbfb8aa3b, v105
	v_rcp_f32_e32 v15, v7
	v_rcp_f32_e32 v7, v4
	v_exp_f32_e32 v2, v2
	v_exp_f32_e32 v3, v3
	v_mul_f32_e32 v4, v13, v20
	v_fmac_f32_e32 v101, v89, v4
	v_mul_f32_e32 v5, v17, v20
	v_mul_f32_e32 v4, 0xbfb8aa3b, v101
	v_fmac_f32_e32 v93, v85, v5
	v_exp_f32_e32 v4, v4
	v_mul_f32_e32 v5, 0xbfb8aa3b, v93
	v_exp_f32_e32 v5, v5
	v_add_f32_e32 v2, 1.0, v2
	v_add_f32_e32 v3, 1.0, v3
	v_rcp_f32_e32 v2, v2
	v_rcp_f32_e32 v3, v3
	v_add_f32_e32 v4, 1.0, v4
	v_rcp_f32_e32 v8, v6
	v_add_f32_e32 v5, 1.0, v5
	v_rcp_f32_e32 v6, v4
	v_rcp_f32_e32 v9, v5
	v_mul_f32_e32 v13, v4, v2
	v_mul_f32_e32 v17, v5, v3
	v_cvt_pk_bf16_f32 v2, v21, v11
	v_cvt_pk_bf16_f32 v3, v7, v6
	v_lshlrev_b64 v[6:7], 12, v[18:19]
	v_cvt_pk_bf16_f32 v4, v22, v15
	v_cvt_pk_bf16_f32 v5, v8, v9
	v_lshl_add_u64 v[8:9], s[16:17], 0, v[6:7]
	v_lshl_add_u64 v[6:7], s[10:11], 0, v[6:7]
	v_lshl_add_u64 v[8:9], v[8:9], 0, v[146:147]
	v_lshl_add_u64 v[6:7], v[6:7], 0, v[146:147]
	global_store_dwordx4 v[8:9], v[2:5], off
	s_nop 1
	v_cvt_pk_bf16_f32 v2, v10, v23
	v_cvt_pk_bf16_f32 v3, v12, v13
	v_cvt_pk_bf16_f32 v4, v14, v24
	v_cvt_pk_bf16_f32 v5, v16, v17
	global_store_dwordx4 v[6:7], v[2:5], off
	s_cbranch_vccnz .LBB0_872
	s_andn2_b64 vcc, exec, s[8:9]
	s_cbranch_vccnz .LBB0_871
	s_barrier
	s_branch .LBB0_871
